# K-loop load segments: ds_read_b128 fragment loads issued first, address VALU / M0 / LDS-DMA after them (docs 6.4 start-of-segment placement)
# speedup vs baseline: 1.0040x; 1.0024x over previous
; #define PG8_STAGE(bufoff, gbase, voff) do { _Pragma("unroll") for (int _i = 0; _i < 2; ++_i) \
;         __builtin_amdgcn_global_load_lds((const unsigned*)((const char*)(gbase) + (voff)[_i]), (PG8_LAS unsigned*)(lds + (bufoff) + ldsw + _i * 8192), 16, 0, 0); } while (0)
; #define PG8_LDA(dst, b, h) do { _Pragma("unroll") for (int m = 0; m < 4; ++m) { const bf16x8 f0_ = *(const PG8_LAS bf16x8*)(lds + PG8_SA(b, h) + aoff + m * 2048), f1_ = *(const PG8_LAS bf16x8*)(lds + PG8_SA(b, h) + aoff + m * 2048 + 1024); dst[m].set(f0_, f1_); } } while (0)
; #define PG8_LDB(dst, b, h) do { _Pragma("unroll") for (int n = 0; n < 2; ++n) { const bf16x8 f0_ = *(const PG8_LAS bf16x8*)(lds + PG8_SB(b, h) + boff + n * 2048), f1_ = *(const PG8_LAS bf16x8*)(lds + PG8_SB(b, h) + boff + n * 2048 + 1024); dst[n].set(f0_, f1_); } } while (0)
; #define PG8_WAIT_V(n) asm volatile("s_waitcnt vmcnt(" #n ")" ::: "memory")
; #define PG8_WAIT_L(n) asm volatile("s_waitcnt lgkmcnt(" #n ")" ::: "memory")
; #define PG8_BAR __builtin_amdgcn_s_barrier()
; #define PG8_SCHED __builtin_amdgcn_sched_barrier(0)
; template <class Epi, class Sched, bool ALIGN_EPI = false, bool SP2 = false>
; __device__ __forceinline__ void gemm_phase(PG8_LAS unsigned char* lds, const Gemm g, const Sched& S, const Epi& E) {
;     ...
;             const bool last = (t == nt - 2);
;             const char* a1 = cA + (size_t)(t + 1) * kstep;
;             const char* a2 = last ? nA : cA + (size_t)(t + 2) * kstep; const char* b2 = last ? nB : cB + (size_t)(t + 2) * kstep;
;             const char* a3 = a2 + kstep; const char* b3 = b2 + kstep;
;             if (last && has_next) S.a_ready(nxt);
;             if constexpr (SP2) {
;             PG8_LDB(B0, 0, 0); PG8_LDB(B1, 0, 1); PG8_SCHED; PG8_LDA(At, 0, 0); PG8_STAGE(PG8_SA(1, 1), a1 + hstep, voffA);
;             PG8_WAIT_V(8); PG8_WAIT_L(0); PG8_BAR; PG8_MMA(0, 0, At, B0); PG8_MMA(0, 1, At, B1); PG8_BAR; PG8_SCHED;
;             PG8_LDA(At, 0, 1); PG8_STAGE(PG8_SB(0, 0), b2, voffB); PG8_STAGE(PG8_SB(0, 1), b2 + hstepB, voffB); PG8_STAGE(PG8_SA(0, 0), a2, voffA);
;             PG8_WAIT_V(8); PG8_WAIT_L(0); PG8_BAR; PG8_MMA(1, 0, At, B0); PG8_MMA(1, 1, At, B1); PG8_BAR; PG8_SCHED;
.LBB0_204:
	ds_read_b128 v[18:21], v203
	ds_read_b128 v[22:25], v203 offset:1024
	ds_read_b128 v[26:29], v203 offset:2048
	ds_read_b128 v[30:33], v203 offset:3072
	ds_read_b128 v[2:5], v204
	ds_read_b128 v[6:9], v204 offset:1024
	ds_read_b128 v[10:13], v204 offset:2048
	ds_read_b128 v[14:17], v204 offset:3072
	ds_read_b128 v[182:185], v205
	ds_read_b128 v[186:189], v205 offset:1024
	ds_read_b128 v[212:215], v205 offset:2048
	ds_read_b128 v[216:219], v205 offset:3072
	ds_read_b128 v[220:223], v205 offset:4096
	ds_read_b128 v[224:227], v205 offset:5120
	ds_read_b128 v[228:231], v205 offset:6144
	ds_read_b128 v[232:235], v205 offset:7168
	s_add_i32 s53, s48, 2
	s_add_u32 s0, s2, 0x80
	s_addc_u32 s1, s3, 0
	s_cmp_eq_u32 s71, s48
	s_cselect_b32 s48, s44, s0
	s_cselect_b32 s49, s45, s1
	s_cselect_b32 s51, s47, s52
	s_cselect_b32 s50, s46, s20
	s_cmp_eq_u32 s99, 0
	s_cbranch_scc1 .Lkr0_a
	v_lshl_add_u64 v[190:191], v[190:191], 0, s[36:37]
	s_mov_b32 m0, s66
	v_lshl_add_u64 v[192:193], v[192:193], 0, s[36:37]
	global_load_lds_dwordx4 v[190:191], off
	s_mov_b32 m0, s67
	s_nop 0
	global_load_lds_dwordx4 v[192:193], off
.Lkr0_a:
	v_lshl_add_u64 v[190:191], s[2:3], 0, v[174:175]
	s_add_i32 m0, s58, 0xc000
	s_nop 0
	global_load_lds_dwordx4 v[190:191], off
	v_lshl_add_u64 v[190:191], s[2:3], 0, v[176:177]
	s_add_i32 m0, s58, 0xe000
	s_nop 0
	global_load_lds_dwordx4 v[190:191], off
	s_waitcnt vmcnt(8)
	s_waitcnt lgkmcnt(0)
	s_barrier
	s_setprio 1
	s_waitcnt lgkmcnt(0)
	v_mfma_scale_f32_16x16x128_f8f6f4 v[158:161], v[18:25], v[182:189], v[158:161], v206, v207 op_sel_hi:[0,0,0]
	v_mfma_scale_f32_16x16x128_f8f6f4 v[154:157], v[26:33], v[182:189], v[154:157], v206, v207 op_sel_hi:[0,0,0]
	v_mfma_scale_f32_16x16x128_f8f6f4 v[142:145], v[18:25], v[212:219], v[142:145], v206, v207 op_sel_hi:[0,0,0]
	v_mfma_scale_f32_16x16x128_f8f6f4 v[138:141], v[26:33], v[212:219], v[138:141], v206, v207 op_sel_hi:[0,0,0]
	v_mfma_scale_f32_16x16x128_f8f6f4 v[126:129], v[18:25], v[220:227], v[126:129], v206, v207 op_sel_hi:[0,0,0]
	v_mfma_scale_f32_16x16x128_f8f6f4 v[122:125], v[26:33], v[220:227], v[122:125], v206, v207 op_sel_hi:[0,0,0]
	v_mfma_scale_f32_16x16x128_f8f6f4 v[110:113], v[18:25], v[228:235], v[110:113], v206, v207 op_sel_hi:[0,0,0]
	v_mfma_scale_f32_16x16x128_f8f6f4 v[106:109], v[26:33], v[228:235], v[106:109], v206, v207 op_sel_hi:[0,0,0]
	s_setprio 0
	s_setprio 1
	v_mfma_scale_f32_16x16x128_f8f6f4 v[150:153], v[2:9], v[182:189], v[150:153], v206, v207 op_sel_hi:[0,0,0]
	v_mfma_scale_f32_16x16x128_f8f6f4 v[146:149], v[10:17], v[182:189], v[146:149], v206, v207 op_sel_hi:[0,0,0]
	v_mfma_scale_f32_16x16x128_f8f6f4 v[134:137], v[2:9], v[212:219], v[134:137], v206, v207 op_sel_hi:[0,0,0]
	v_mfma_scale_f32_16x16x128_f8f6f4 v[130:133], v[10:17], v[212:219], v[130:133], v206, v207 op_sel_hi:[0,0,0]
	v_mfma_scale_f32_16x16x128_f8f6f4 v[118:121], v[2:9], v[220:227], v[118:121], v206, v207 op_sel_hi:[0,0,0]
	v_mfma_scale_f32_16x16x128_f8f6f4 v[114:117], v[10:17], v[220:227], v[114:117], v206, v207 op_sel_hi:[0,0,0]
	v_mfma_scale_f32_16x16x128_f8f6f4 v[102:105], v[2:9], v[228:235], v[102:105], v206, v207 op_sel_hi:[0,0,0]
	v_mfma_scale_f32_16x16x128_f8f6f4 v[98:101], v[10:17], v[228:235], v[98:101], v206, v207 op_sel_hi:[0,0,0]
	s_setprio 0
	s_barrier
	ds_read_b128 v[212:215], v205 offset:16384
	ds_read_b128 v[216:219], v205 offset:17408
	ds_read_b128 v[220:223], v205 offset:18432
	ds_read_b128 v[224:227], v205 offset:19456
	ds_read_b128 v[228:231], v205 offset:20480
	ds_read_b128 v[232:235], v205 offset:21504
	ds_read_b128 v[236:239], v205 offset:22528
	ds_read_b128 v[240:243], v205 offset:23552
	s_add_i32 s0, s76, s57
	v_lshl_add_u64 v[182:183], s[50:51], 0, v[164:165]
	s_mov_b32 m0, s0
	s_nop 0
	global_load_lds_dwordx4 v[182:183], off
	s_add_i32 m0, s0, 0x2000
	v_lshl_add_u64 v[184:185], s[50:51], 0, v[168:169]
	s_add_u32 s50, s50, s16
	s_addc_u32 s51, s51, s17
	s_add_i32 s0, s77, s57
	global_load_lds_dwordx4 v[184:185], off
	v_lshl_add_u64 v[186:187], s[50:51], 0, v[164:165]
	s_mov_b32 m0, s0
	v_lshl_add_u64 v[188:189], s[50:51], 0, v[168:169]
	global_load_lds_dwordx4 v[186:187], off
	s_add_i32 m0, s0, 0x2000
	v_lshl_add_u64 v[190:191], s[48:49], 0, v[162:163]
	global_load_lds_dwordx4 v[188:189], off
	v_lshl_add_u64 v[192:193], s[48:49], 0, v[166:167]
	s_waitcnt vmcnt(6)
	s_waitcnt lgkmcnt(0)
	s_barrier
; #define PG8_STAGE(bufoff, gbase, voff) do { _Pragma("unroll") for (int _i = 0; _i < 2; ++_i) \
;         __builtin_amdgcn_global_load_lds((const unsigned*)((const char*)(gbase) + (voff)[_i]), (PG8_LAS unsigned*)(lds + (bufoff) + ldsw + _i * 8192), 16, 0, 0); } while (0)
; #define PG8_LDA(dst, b, h) do { _Pragma("unroll") for (int m = 0; m < 4; ++m) { const bf16x8 f0_ = *(const PG8_LAS bf16x8*)(lds + PG8_SA(b, h) + aoff + m * 2048), f1_ = *(const PG8_LAS bf16x8*)(lds + PG8_SA(b, h) + aoff + m * 2048 + 1024); dst[m].set(f0_, f1_); } } while (0)
; #define PG8_LDB(dst, b, h) do { _Pragma("unroll") for (int n = 0; n < 2; ++n) { const bf16x8 f0_ = *(const PG8_LAS bf16x8*)(lds + PG8_SB(b, h) + boff + n * 2048), f1_ = *(const PG8_LAS bf16x8*)(lds + PG8_SB(b, h) + boff + n * 2048 + 1024); dst[n].set(f0_, f1_); } } while (0)
; #define PG8_WAIT_V(n) asm volatile("s_waitcnt vmcnt(" #n ")" ::: "memory")
; #define PG8_WAIT_L(n) asm volatile("s_waitcnt lgkmcnt(" #n ")" ::: "memory")
; #define PG8_BAR __builtin_amdgcn_s_barrier()
; #define PG8_SCHED __builtin_amdgcn_sched_barrier(0)
; template <class Epi, class Sched, bool ALIGN_EPI = false, bool SP2 = false>
; __device__ __forceinline__ void gemm_phase(PG8_LAS unsigned char* lds, const Gemm g, const Sched& S, const Epi& E) {
;     ...
;             PG8_WAIT_V(8); PG8_WAIT_L(0); PG8_BAR; PG8_MMA(1, 0, At, B0); PG8_MMA(1, 1, At, B1); PG8_BAR; PG8_SCHED;
;             PG8_LDB(B0, 1, 0); PG8_LDB(B1, 1, 1); PG8_SCHED; PG8_LDA(At, 1, 0); PG8_STAGE(PG8_SA(0, 1), a2 + hstep, voffA);
;             PG8_WAIT_V(8); PG8_WAIT_L(0); PG8_BAR; PG8_MMA(0, 0, At, B0); PG8_MMA(0, 1, At, B1); PG8_BAR; PG8_SCHED;
;             PG8_LDA(At, 1, 1); PG8_STAGE(PG8_SB(1, 0), b3, voffB); PG8_STAGE(PG8_SB(1, 1), b3 + hstepB, voffB); PG8_STAGE(PG8_SA(1, 0), a3, voffA);
;             PG8_WAIT_V(8); PG8_WAIT_L(0); PG8_BAR; PG8_MMA(1, 0, At, B0); PG8_MMA(1, 1, At, B1); PG8_BAR; PG8_SCHED;
	s_setprio 1
	s_waitcnt lgkmcnt(0)
	v_mfma_scale_f32_16x16x128_f8f6f4 v[94:97], v[18:25], v[212:219], v[94:97], v206, v207 op_sel_hi:[0,0,0]
	v_mfma_scale_f32_16x16x128_f8f6f4 v[90:93], v[26:33], v[212:219], v[90:93], v206, v207 op_sel_hi:[0,0,0]
	v_mfma_scale_f32_16x16x128_f8f6f4 v[78:81], v[18:25], v[220:227], v[78:81], v206, v207 op_sel_hi:[0,0,0]
	v_mfma_scale_f32_16x16x128_f8f6f4 v[74:77], v[26:33], v[220:227], v[74:77], v206, v207 op_sel_hi:[0,0,0]
	v_mfma_scale_f32_16x16x128_f8f6f4 v[62:65], v[18:25], v[228:235], v[62:65], v206, v207 op_sel_hi:[0,0,0]
	v_mfma_scale_f32_16x16x128_f8f6f4 v[58:61], v[26:33], v[228:235], v[58:61], v206, v207 op_sel_hi:[0,0,0]
	v_mfma_scale_f32_16x16x128_f8f6f4 v[46:49], v[18:25], v[236:243], v[46:49], v206, v207 op_sel_hi:[0,0,0]
	v_mfma_scale_f32_16x16x128_f8f6f4 v[42:45], v[26:33], v[236:243], v[42:45], v206, v207 op_sel_hi:[0,0,0]
	s_setprio 0
	s_setprio 1
	v_mfma_scale_f32_16x16x128_f8f6f4 v[86:89], v[2:9], v[212:219], v[86:89], v206, v207 op_sel_hi:[0,0,0]
	v_mfma_scale_f32_16x16x128_f8f6f4 v[82:85], v[10:17], v[212:219], v[82:85], v206, v207 op_sel_hi:[0,0,0]
	v_mfma_scale_f32_16x16x128_f8f6f4 v[70:73], v[2:9], v[220:227], v[70:73], v206, v207 op_sel_hi:[0,0,0]
	v_mfma_scale_f32_16x16x128_f8f6f4 v[66:69], v[10:17], v[220:227], v[66:69], v206, v207 op_sel_hi:[0,0,0]
	v_mfma_scale_f32_16x16x128_f8f6f4 v[54:57], v[2:9], v[228:235], v[54:57], v206, v207 op_sel_hi:[0,0,0]
	v_mfma_scale_f32_16x16x128_f8f6f4 v[50:53], v[10:17], v[228:235], v[50:53], v206, v207 op_sel_hi:[0,0,0]
	v_mfma_scale_f32_16x16x128_f8f6f4 v[38:41], v[2:9], v[236:243], v[38:41], v206, v207 op_sel_hi:[0,0,0]
	v_mfma_scale_f32_16x16x128_f8f6f4 v[34:37], v[10:17], v[236:243], v[34:37], v206, v207 op_sel_hi:[0,0,0]
	s_setprio 0
	s_barrier
	ds_read_b128 v[212:215], v205 offset:32768
	ds_read_b128 v[216:219], v205 offset:33792
	ds_read_b128 v[220:223], v205 offset:34816
	ds_read_b128 v[224:227], v205 offset:35840
	ds_read_b128 v[228:231], v205 offset:36864
	ds_read_b128 v[232:235], v205 offset:37888
	ds_read_b128 v[236:239], v205 offset:38912
	ds_read_b128 v[240:243], v205 offset:39936
	s_add_i32 s0, 0, 0x18000
	s_add_i32 s1, 0, 0x1c000
	v_add_u32_e32 v14, s0, v194
	v_add_u32_e32 v30, s1, v194
	ds_read_b128 v[2:5], v14
	ds_read_b128 v[6:9], v14 offset:1024
	ds_read_b128 v[10:13], v14 offset:2048
	ds_read_b128 v[14:17], v14 offset:3072
	ds_read_b128 v[18:21], v30
	ds_read_b128 v[22:25], v30 offset:1024
	ds_read_b128 v[26:29], v30 offset:2048
	ds_read_b128 v[30:33], v30 offset:3072
	s_add_u32 s48, s48, s14
	s_addc_u32 s49, s49, s15
	s_mov_b32 m0, s61
	v_lshl_add_u64 v[244:245], s[48:49], 0, v[162:163]
	s_mov_b32 m0, s58
	s_nop 0
	global_load_lds_dwordx4 v[190:191], off
	s_mov_b32 m0, s59
	s_nop 0
	global_load_lds_dwordx4 v[192:193], off
	s_mov_b32 m0, s61
	s_nop 0
	global_load_lds_dwordx4 v[244:245], off
	v_lshl_add_u64 v[244:245], s[48:49], 0, v[166:167]
	s_mov_b32 m0, s63
	s_nop 0
	global_load_lds_dwordx4 v[244:245], off
	s_waitcnt vmcnt(8)
	s_waitcnt lgkmcnt(0)
	s_barrier
	s_setprio 1
	s_waitcnt lgkmcnt(0)
	v_mfma_scale_f32_16x16x128_f8f6f4 v[158:161], v[2:9], v[212:219], v[158:161], v206, v207 op_sel_hi:[0,0,0]
	v_mfma_scale_f32_16x16x128_f8f6f4 v[154:157], v[10:17], v[212:219], v[154:157], v206, v207 op_sel_hi:[0,0,0]
	v_mfma_scale_f32_16x16x128_f8f6f4 v[142:145], v[2:9], v[220:227], v[142:145], v206, v207 op_sel_hi:[0,0,0]
	v_mfma_scale_f32_16x16x128_f8f6f4 v[138:141], v[10:17], v[220:227], v[138:141], v206, v207 op_sel_hi:[0,0,0]
	v_mfma_scale_f32_16x16x128_f8f6f4 v[126:129], v[2:9], v[228:235], v[126:129], v206, v207 op_sel_hi:[0,0,0]
	v_mfma_scale_f32_16x16x128_f8f6f4 v[122:125], v[10:17], v[228:235], v[122:125], v206, v207 op_sel_hi:[0,0,0]
	v_mfma_scale_f32_16x16x128_f8f6f4 v[110:113], v[2:9], v[236:243], v[110:113], v206, v207 op_sel_hi:[0,0,0]
	v_mfma_scale_f32_16x16x128_f8f6f4 v[106:109], v[10:17], v[236:243], v[106:109], v206, v207 op_sel_hi:[0,0,0]
	s_setprio 0
	s_setprio 1
	v_mfma_scale_f32_16x16x128_f8f6f4 v[150:153], v[18:25], v[212:219], v[150:153], v206, v207 op_sel_hi:[0,0,0]
	v_mfma_scale_f32_16x16x128_f8f6f4 v[146:149], v[26:33], v[212:219], v[146:149], v206, v207 op_sel_hi:[0,0,0]
	v_mfma_scale_f32_16x16x128_f8f6f4 v[134:137], v[18:25], v[220:227], v[134:137], v206, v207 op_sel_hi:[0,0,0]
	v_mfma_scale_f32_16x16x128_f8f6f4 v[130:133], v[26:33], v[220:227], v[130:133], v206, v207 op_sel_hi:[0,0,0]
	v_mfma_scale_f32_16x16x128_f8f6f4 v[118:121], v[18:25], v[228:235], v[118:121], v206, v207 op_sel_hi:[0,0,0]
	v_mfma_scale_f32_16x16x128_f8f6f4 v[114:117], v[26:33], v[228:235], v[114:117], v206, v207 op_sel_hi:[0,0,0]
	v_mfma_scale_f32_16x16x128_f8f6f4 v[102:105], v[18:25], v[236:243], v[102:105], v206, v207 op_sel_hi:[0,0,0]
	v_mfma_scale_f32_16x16x128_f8f6f4 v[98:101], v[26:33], v[236:243], v[98:101], v206, v207 op_sel_hi:[0,0,0]
	s_setprio 0
	s_barrier
	ds_read_b128 v[212:215], v205 offset:49152
	ds_read_b128 v[216:219], v205 offset:50176
	ds_read_b128 v[220:223], v205 offset:51200
	ds_read_b128 v[224:227], v205 offset:52224
	ds_read_b128 v[228:231], v205 offset:53248
	ds_read_b128 v[232:235], v205 offset:54272
	ds_read_b128 v[236:239], v205 offset:55296
	ds_read_b128 v[240:243], v205 offset:56320
	s_add_i32 s0, s0, s57
	v_lshl_add_u64 v[182:183], v[182:183], 0, s[36:37]
	s_mov_b32 m0, s0
	s_nop 0
	global_load_lds_dwordx4 v[182:183], off
	v_lshl_add_u64 v[182:183], v[184:185], 0, s[36:37]
	s_add_i32 m0, s0, 0x2000
	s_add_i32 s0, s1, s57
	global_load_lds_dwordx4 v[182:183], off
	v_lshl_add_u64 v[182:183], v[186:187], 0, s[36:37]
	s_mov_b32 m0, s0
	s_nop 0
	global_load_lds_dwordx4 v[182:183], off
	v_lshl_add_u64 v[182:183], v[188:189], 0, s[36:37]
	s_add_i32 m0, s0, 0x2000
	s_nop 0
	global_load_lds_dwordx4 v[182:183], off
	s_cmp_ge_i32 s53, s69
	s_cbranch_scc0 .Lkr0_b
	v_lshl_add_u64 v[182:183], v[190:191], 0, s[36:37]
	s_mov_b32 m0, s66
	s_nop 0
	global_load_lds_dwordx4 v[182:183], off
	v_lshl_add_u64 v[182:183], v[192:193], 0, s[36:37]
	s_mov_b32 m0, s67
	s_nop 0
	global_load_lds_dwordx4 v[182:183], off

; #define PG8_STAGE(bufoff, gbase, voff) do { _Pragma("unroll") for (int _i = 0; _i < 2; ++_i) \
;         __builtin_amdgcn_global_load_lds((const unsigned*)((const char*)(gbase) + (voff)[_i]), (PG8_LAS unsigned*)(lds + (bufoff) + ldsw + _i * 8192), 16, 0, 0); } while (0)
; #define PG8_LDA(dst, b, h) do { _Pragma("unroll") for (int m = 0; m < 4; ++m) { const bf16x8 f0_ = *(const PG8_LAS bf16x8*)(lds + PG8_SA(b, h) + aoff + m * 2048), f1_ = *(const PG8_LAS bf16x8*)(lds + PG8_SA(b, h) + aoff + m * 2048 + 1024); dst[m].set(f0_, f1_); } } while (0)
; #define PG8_LDB(dst, b, h) do { _Pragma("unroll") for (int n = 0; n < 2; ++n) { const bf16x8 f0_ = *(const PG8_LAS bf16x8*)(lds + PG8_SB(b, h) + boff + n * 2048), f1_ = *(const PG8_LAS bf16x8*)(lds + PG8_SB(b, h) + boff + n * 2048 + 1024); dst[n].set(f0_, f1_); } } while (0)
; #define PG8_WAIT_V(n) asm volatile("s_waitcnt vmcnt(" #n ")" ::: "memory")
; #define PG8_WAIT_L(n) asm volatile("s_waitcnt lgkmcnt(" #n ")" ::: "memory")
; #define PG8_BAR __builtin_amdgcn_s_barrier()
; #define PG8_SCHED __builtin_amdgcn_sched_barrier(0)
; template <class Epi, class Sched, bool ALIGN_EPI = false, bool SP2 = false>
; __device__ __forceinline__ void gemm_phase(PG8_LAS unsigned char* lds, const Gemm g, const Sched& S, const Epi& E) {
;     ...
;             const bool last = (t == nt - 2);
;             const char* a1 = cA + (size_t)(t + 1) * kstep;
;             const char* a2 = last ? nA : cA + (size_t)(t + 2) * kstep; const char* b2 = last ? nB : cB + (size_t)(t + 2) * kstep;
;             const char* a3 = a2 + kstep; const char* b3 = b2 + kstep;
;             if (last && has_next) S.a_ready(nxt);
;             if constexpr (SP2) {
;             PG8_LDB(B0, 0, 0); PG8_LDB(B1, 0, 1); PG8_SCHED; PG8_LDA(At, 0, 0); PG8_STAGE(PG8_SA(1, 1), a1 + hstep, voffA);
;             PG8_WAIT_V(8); PG8_WAIT_L(0); PG8_BAR; PG8_MMA(0, 0, At, B0); PG8_MMA(0, 1, At, B1); PG8_BAR; PG8_SCHED;
;             PG8_LDA(At, 0, 1); PG8_STAGE(PG8_SB(0, 0), b2, voffB); PG8_STAGE(PG8_SB(0, 1), b2 + hstepB, voffB); PG8_STAGE(PG8_SA(0, 0), a2, voffA);
;             PG8_WAIT_V(8); PG8_WAIT_L(0); PG8_BAR; PG8_MMA(1, 0, At, B0); PG8_MMA(1, 1, At, B1); PG8_BAR; PG8_SCHED;
.LBB0_984:
	ds_read_b128 v[206:209], v176
	ds_read_b128 v[212:215], v176 offset:1024
	ds_read_b128 v[216:219], v176 offset:2048
	ds_read_b128 v[220:223], v176 offset:3072
	ds_read_b128 v[224:227], v176 offset:4096
	ds_read_b128 v[228:231], v176 offset:5120
	ds_read_b128 v[232:235], v176 offset:6144
	ds_read_b128 v[236:239], v176 offset:7168
	s_add_i32 s75, s42, 2
	v_add_u32_e32 v186, s59, v173
	v_add_u32_e32 v202, s61, v173
	s_add_u32 s0, s38, s40
	ds_read_b128 v[168:171], v186
	ds_read_b128 v[178:181], v186 offset:1024
	ds_read_b128 v[182:185], v186 offset:2048
	ds_read_b128 v[186:189], v186 offset:3072
	ds_read_b128 v[190:193], v202
	ds_read_b128 v[194:197], v202 offset:1024
	ds_read_b128 v[198:201], v202 offset:2048
	ds_read_b128 v[202:205], v202 offset:3072
	s_addc_u32 s1, s39, s41
	s_add_u32 s0, s0, 0x100
	s_addc_u32 s1, s1, 0
	s_add_u32 s33, s73, s40
	s_addc_u32 s76, s74, s41
	s_cmp_eq_u32 s57, s42
	s_cselect_b32 s43, s3, s1
	s_cselect_b32 s42, s2, s0
	s_cselect_b32 s1, s37, s76
	s_cselect_b32 s0, s36, s33
	v_lshl_add_u64 v[240:241], v[164:165], 0, s[40:41]
	s_add_i32 m0, s47, 0xc000
	s_nop 0
	global_load_lds_dwordx4 v[240:241], off
	v_lshl_add_u64 v[240:241], v[166:167], 0, s[40:41]
	s_add_i32 m0, s47, 0xe000
	s_nop 0
	global_load_lds_dwordx4 v[240:241], off
	s_waitcnt vmcnt(8)
	s_waitcnt lgkmcnt(0)
	s_barrier
	s_setprio 1
	s_waitcnt lgkmcnt(0)
	v_mfma_f32_16x16x32_bf16 v[126:129], v[168:171], v[206:209], v[126:129]
	v_mfma_f32_16x16x32_bf16 v[122:125], v[182:185], v[206:209], v[122:125]
	v_mfma_f32_16x16x32_bf16 v[110:113], v[168:171], v[216:219], v[110:113]
	v_mfma_f32_16x16x32_bf16 v[106:109], v[182:185], v[216:219], v[106:109]
	v_mfma_f32_16x16x32_bf16 v[94:97], v[168:171], v[224:227], v[94:97]
	v_mfma_f32_16x16x32_bf16 v[90:93], v[182:185], v[224:227], v[90:93]
	v_mfma_f32_16x16x32_bf16 v[78:81], v[168:171], v[232:235], v[78:81]
	v_mfma_f32_16x16x32_bf16 v[74:77], v[182:185], v[232:235], v[74:77]
	v_mfma_f32_16x16x32_bf16 v[126:129], v[178:181], v[212:215], v[126:129]
	v_mfma_f32_16x16x32_bf16 v[122:125], v[186:189], v[212:215], v[122:125]
	v_mfma_f32_16x16x32_bf16 v[110:113], v[178:181], v[220:223], v[110:113]
	v_mfma_f32_16x16x32_bf16 v[106:109], v[186:189], v[220:223], v[106:109]
	v_mfma_f32_16x16x32_bf16 v[94:97], v[178:181], v[228:231], v[94:97]
	v_mfma_f32_16x16x32_bf16 v[90:93], v[186:189], v[228:231], v[90:93]
	v_mfma_f32_16x16x32_bf16 v[78:81], v[178:181], v[236:239], v[78:81]
	v_mfma_f32_16x16x32_bf16 v[74:77], v[186:189], v[236:239], v[74:77]
	s_setprio 0
	s_setprio 1
	v_mfma_f32_16x16x32_bf16 v[118:121], v[190:193], v[206:209], v[118:121]
	v_mfma_f32_16x16x32_bf16 v[114:117], v[198:201], v[206:209], v[114:117]
	v_mfma_f32_16x16x32_bf16 v[102:105], v[190:193], v[216:219], v[102:105]
	v_mfma_f32_16x16x32_bf16 v[98:101], v[198:201], v[216:219], v[98:101]
	v_mfma_f32_16x16x32_bf16 v[86:89], v[190:193], v[224:227], v[86:89]
	v_mfma_f32_16x16x32_bf16 v[82:85], v[198:201], v[224:227], v[82:85]
	v_mfma_f32_16x16x32_bf16 v[70:73], v[190:193], v[232:235], v[70:73]
	v_mfma_f32_16x16x32_bf16 v[66:69], v[198:201], v[232:235], v[66:69]
	v_mfma_f32_16x16x32_bf16 v[118:121], v[194:197], v[212:215], v[118:121]
	v_mfma_f32_16x16x32_bf16 v[114:117], v[202:205], v[212:215], v[114:117]
	v_mfma_f32_16x16x32_bf16 v[102:105], v[194:197], v[220:223], v[102:105]
	v_mfma_f32_16x16x32_bf16 v[98:101], v[202:205], v[220:223], v[98:101]
	v_mfma_f32_16x16x32_bf16 v[86:89], v[194:197], v[228:231], v[86:89]
	v_mfma_f32_16x16x32_bf16 v[82:85], v[202:205], v[228:231], v[82:85]
	v_mfma_f32_16x16x32_bf16 v[70:73], v[194:197], v[236:239], v[70:73]
	v_mfma_f32_16x16x32_bf16 v[66:69], v[202:205], v[236:239], v[66:69]
	s_setprio 0
	s_barrier
	ds_read_b128 v[206:209], v176 offset:16384
	ds_read_b128 v[212:215], v176 offset:17408
	ds_read_b128 v[216:219], v176 offset:18432
	ds_read_b128 v[220:223], v176 offset:19456
	ds_read_b128 v[224:227], v176 offset:20480
	ds_read_b128 v[228:231], v176 offset:21504
	ds_read_b128 v[232:235], v176 offset:22528
	ds_read_b128 v[236:239], v176 offset:23552
	s_add_i32 s33, s59, s46
	v_lshl_add_u64 v[240:241], s[0:1], 0, v[132:133]
	s_mov_b32 m0, s33
	s_nop 0
	global_load_lds_dwordx4 v[240:241], off
	s_add_i32 m0, s33, 0x2000
	v_lshl_add_u64 v[242:243], s[0:1], 0, v[136:137]
	s_add_u32 s0, s0, s14
	s_addc_u32 s1, s1, s15
	s_add_i32 s33, s61, s46
	global_load_lds_dwordx4 v[242:243], off
	v_lshl_add_u64 v[244:245], s[0:1], 0, v[132:133]
	s_mov_b32 m0, s33
	v_lshl_add_u64 v[246:247], s[0:1], 0, v[136:137]
	global_load_lds_dwordx4 v[244:245], off
	s_add_i32 m0, s33, 0x2000
	v_lshl_add_u64 v[248:249], s[42:43], 0, v[130:131]
	global_load_lds_dwordx4 v[246:247], off
	v_lshl_add_u64 v[250:251], s[42:43], 0, v[134:135]
	s_waitcnt vmcnt(6)
	s_waitcnt lgkmcnt(0)
	s_barrier
; #define PG8_STAGE(bufoff, gbase, voff) do { _Pragma("unroll") for (int _i = 0; _i < 2; ++_i) \
;         __builtin_amdgcn_global_load_lds((const unsigned*)((const char*)(gbase) + (voff)[_i]), (PG8_LAS unsigned*)(lds + (bufoff) + ldsw + _i * 8192), 16, 0, 0); } while (0)
; #define PG8_LDA(dst, b, h) do { _Pragma("unroll") for (int m = 0; m < 4; ++m) { const bf16x8 f0_ = *(const PG8_LAS bf16x8*)(lds + PG8_SA(b, h) + aoff + m * 2048), f1_ = *(const PG8_LAS bf16x8*)(lds + PG8_SA(b, h) + aoff + m * 2048 + 1024); dst[m].set(f0_, f1_); } } while (0)
; #define PG8_LDB(dst, b, h) do { _Pragma("unroll") for (int n = 0; n < 2; ++n) { const bf16x8 f0_ = *(const PG8_LAS bf16x8*)(lds + PG8_SB(b, h) + boff + n * 2048), f1_ = *(const PG8_LAS bf16x8*)(lds + PG8_SB(b, h) + boff + n * 2048 + 1024); dst[n].set(f0_, f1_); } } while (0)
; #define PG8_WAIT_V(n) asm volatile("s_waitcnt vmcnt(" #n ")" ::: "memory")
; #define PG8_WAIT_L(n) asm volatile("s_waitcnt lgkmcnt(" #n ")" ::: "memory")
; #define PG8_BAR __builtin_amdgcn_s_barrier()
; #define PG8_SCHED __builtin_amdgcn_sched_barrier(0)
; template <class Epi, class Sched, bool ALIGN_EPI = false, bool SP2 = false>
; __device__ __forceinline__ void gemm_phase(PG8_LAS unsigned char* lds, const Gemm g, const Sched& S, const Epi& E) {
;     ...
;             PG8_WAIT_V(8); PG8_WAIT_L(0); PG8_BAR; PG8_MMA(1, 0, At, B0); PG8_MMA(1, 1, At, B1); PG8_BAR; PG8_SCHED;
;             PG8_LDB(B0, 1, 0); PG8_LDB(B1, 1, 1); PG8_SCHED; PG8_LDA(At, 1, 0); PG8_STAGE(PG8_SA(0, 1), a2 + hstep, voffA);
;             PG8_WAIT_V(8); PG8_WAIT_L(0); PG8_BAR; PG8_MMA(0, 0, At, B0); PG8_MMA(0, 1, At, B1); PG8_BAR; PG8_SCHED;
	s_setprio 1
	s_waitcnt lgkmcnt(0)
	v_mfma_f32_16x16x32_bf16 v[62:65], v[168:171], v[206:209], v[62:65]
	v_mfma_f32_16x16x32_bf16 v[58:61], v[182:185], v[206:209], v[58:61]
	v_mfma_f32_16x16x32_bf16 v[46:49], v[168:171], v[216:219], v[46:49]
	v_mfma_f32_16x16x32_bf16 v[42:45], v[182:185], v[216:219], v[42:45]
	v_mfma_f32_16x16x32_bf16 v[30:33], v[168:171], v[224:227], v[30:33]
	v_mfma_f32_16x16x32_bf16 v[26:29], v[182:185], v[224:227], v[26:29]
	v_mfma_f32_16x16x32_bf16 v[14:17], v[168:171], v[232:235], v[14:17]
	v_mfma_f32_16x16x32_bf16 v[10:13], v[182:185], v[232:235], v[10:13]
	v_mfma_f32_16x16x32_bf16 v[62:65], v[178:181], v[212:215], v[62:65]
	v_mfma_f32_16x16x32_bf16 v[58:61], v[186:189], v[212:215], v[58:61]
	v_mfma_f32_16x16x32_bf16 v[46:49], v[178:181], v[220:223], v[46:49]
	v_mfma_f32_16x16x32_bf16 v[42:45], v[186:189], v[220:223], v[42:45]
	v_mfma_f32_16x16x32_bf16 v[30:33], v[178:181], v[228:231], v[30:33]
	v_mfma_f32_16x16x32_bf16 v[26:29], v[186:189], v[228:231], v[26:29]
	v_mfma_f32_16x16x32_bf16 v[14:17], v[178:181], v[236:239], v[14:17]
	v_mfma_f32_16x16x32_bf16 v[10:13], v[186:189], v[236:239], v[10:13]
	s_setprio 0
	s_setprio 1
	v_mfma_f32_16x16x32_bf16 v[54:57], v[190:193], v[206:209], v[54:57]
	v_mfma_f32_16x16x32_bf16 v[50:53], v[198:201], v[206:209], v[50:53]
	v_mfma_f32_16x16x32_bf16 v[38:41], v[190:193], v[216:219], v[38:41]
	v_mfma_f32_16x16x32_bf16 v[34:37], v[198:201], v[216:219], v[34:37]
	v_mfma_f32_16x16x32_bf16 v[22:25], v[190:193], v[224:227], v[22:25]
	v_mfma_f32_16x16x32_bf16 v[18:21], v[198:201], v[224:227], v[18:21]
	v_mfma_f32_16x16x32_bf16 v[6:9], v[190:193], v[232:235], v[6:9]
	v_mfma_f32_16x16x32_bf16 v[2:5], v[198:201], v[232:235], v[2:5]
	v_mfma_f32_16x16x32_bf16 v[54:57], v[194:197], v[212:215], v[54:57]
	v_mfma_f32_16x16x32_bf16 v[50:53], v[202:205], v[212:215], v[50:53]
	v_mfma_f32_16x16x32_bf16 v[38:41], v[194:197], v[220:223], v[38:41]
	v_mfma_f32_16x16x32_bf16 v[34:37], v[202:205], v[220:223], v[34:37]
	v_mfma_f32_16x16x32_bf16 v[22:25], v[194:197], v[228:231], v[22:25]
	v_mfma_f32_16x16x32_bf16 v[18:21], v[202:205], v[228:231], v[18:21]
	v_mfma_f32_16x16x32_bf16 v[6:9], v[194:197], v[236:239], v[6:9]
	v_mfma_f32_16x16x32_bf16 v[2:5], v[202:205], v[236:239], v[2:5]
	s_setprio 0
	s_barrier
	ds_read_b128 v[206:209], v176 offset:32768
	ds_read_b128 v[212:215], v176 offset:33792
	ds_read_b128 v[216:219], v176 offset:34816
	ds_read_b128 v[220:223], v176 offset:35840
	ds_read_b128 v[224:227], v176 offset:36864
	ds_read_b128 v[228:231], v176 offset:37888
	ds_read_b128 v[232:235], v176 offset:38912
	ds_read_b128 v[236:239], v176 offset:39936
	s_add_i32 s33, 0, 0x18000
	s_add_i32 s76, 0, 0x1c000
	v_add_u32_e32 v186, s33, v173
	v_add_u32_e32 v202, s76, v173
	ds_read_b128 v[168:171], v186
	ds_read_b128 v[178:181], v186 offset:1024
	ds_read_b128 v[182:185], v186 offset:2048
	ds_read_b128 v[186:189], v186 offset:3072
	ds_read_b128 v[190:193], v202
	ds_read_b128 v[194:197], v202 offset:1024
	ds_read_b128 v[198:201], v202 offset:2048
	ds_read_b128 v[202:205], v202 offset:3072
	s_add_u32 s0, s42, s12
	s_addc_u32 s1, s43, s13
	s_mov_b32 m0, s49
	v_lshl_add_u64 v[252:253], s[0:1], 0, v[130:131]
	s_mov_b32 m0, s47
	s_nop 0
	global_load_lds_dwordx4 v[248:249], off
	s_mov_b32 m0, s48
	s_nop 0
	global_load_lds_dwordx4 v[250:251], off
	s_mov_b32 m0, s49
	s_nop 0
	global_load_lds_dwordx4 v[252:253], off
	v_lshl_add_u64 v[252:253], s[0:1], 0, v[134:135]
	s_mov_b32 m0, s50
	s_nop 0
	global_load_lds_dwordx4 v[252:253], off
	s_waitcnt vmcnt(8)
	s_waitcnt lgkmcnt(0)
	s_barrier
; #define PG8_STAGE(bufoff, gbase, voff) do { _Pragma("unroll") for (int _i = 0; _i < 2; ++_i) \
;         __builtin_amdgcn_global_load_lds((const unsigned*)((const char*)(gbase) + (voff)[_i]), (PG8_LAS unsigned*)(lds + (bufoff) + ldsw + _i * 8192), 16, 0, 0); } while (0)
; #define PG8_LDA(dst, b, h) do { _Pragma("unroll") for (int m = 0; m < 4; ++m) { const bf16x8 f0_ = *(const PG8_LAS bf16x8*)(lds + PG8_SA(b, h) + aoff + m * 2048), f1_ = *(const PG8_LAS bf16x8*)(lds + PG8_SA(b, h) + aoff + m * 2048 + 1024); dst[m].set(f0_, f1_); } } while (0)
; #define PG8_WAIT_V(n) asm volatile("s_waitcnt vmcnt(" #n ")" ::: "memory")
; #define PG8_WAIT_L(n) asm volatile("s_waitcnt lgkmcnt(" #n ")" ::: "memory")
; #define PG8_BAR __builtin_amdgcn_s_barrier()
; #define PG8_SCHED __builtin_amdgcn_sched_barrier(0)
; template <class Epi, class Sched, bool ALIGN_EPI = false, bool SP2 = false>
; __device__ __forceinline__ void gemm_phase(PG8_LAS unsigned char* lds, const Gemm g, const Sched& S, const Epi& E) {
;     ...
;             PG8_WAIT_V(8); PG8_WAIT_L(0); PG8_BAR; PG8_MMA(0, 0, At, B0); PG8_MMA(0, 1, At, B1); PG8_BAR; PG8_SCHED;
;             PG8_LDA(At, 1, 1); PG8_STAGE(PG8_SB(1, 0), b3, voffB); PG8_STAGE(PG8_SB(1, 1), b3 + hstepB, voffB); PG8_STAGE(PG8_SA(1, 0), a3, voffA);
;             PG8_WAIT_V(8); PG8_WAIT_L(0); PG8_BAR; PG8_MMA(1, 0, At, B0); PG8_MMA(1, 1, At, B1); PG8_BAR; PG8_SCHED;
	s_setprio 1
	s_waitcnt lgkmcnt(0)
	v_mfma_f32_16x16x32_bf16 v[126:129], v[168:171], v[206:209], v[126:129]
	v_mfma_f32_16x16x32_bf16 v[122:125], v[182:185], v[206:209], v[122:125]
	v_mfma_f32_16x16x32_bf16 v[110:113], v[168:171], v[216:219], v[110:113]
	v_mfma_f32_16x16x32_bf16 v[106:109], v[182:185], v[216:219], v[106:109]
	v_mfma_f32_16x16x32_bf16 v[94:97], v[168:171], v[224:227], v[94:97]
	v_mfma_f32_16x16x32_bf16 v[90:93], v[182:185], v[224:227], v[90:93]
	v_mfma_f32_16x16x32_bf16 v[78:81], v[168:171], v[232:235], v[78:81]
	v_mfma_f32_16x16x32_bf16 v[74:77], v[182:185], v[232:235], v[74:77]
	v_mfma_f32_16x16x32_bf16 v[126:129], v[178:181], v[212:215], v[126:129]
	v_mfma_f32_16x16x32_bf16 v[122:125], v[186:189], v[212:215], v[122:125]
	v_mfma_f32_16x16x32_bf16 v[110:113], v[178:181], v[220:223], v[110:113]
	v_mfma_f32_16x16x32_bf16 v[106:109], v[186:189], v[220:223], v[106:109]
	v_mfma_f32_16x16x32_bf16 v[94:97], v[178:181], v[228:231], v[94:97]
	v_mfma_f32_16x16x32_bf16 v[90:93], v[186:189], v[228:231], v[90:93]
	v_mfma_f32_16x16x32_bf16 v[78:81], v[178:181], v[236:239], v[78:81]
	v_mfma_f32_16x16x32_bf16 v[74:77], v[186:189], v[236:239], v[74:77]
	s_setprio 0
	s_setprio 1
	v_mfma_f32_16x16x32_bf16 v[118:121], v[190:193], v[206:209], v[118:121]
	v_mfma_f32_16x16x32_bf16 v[114:117], v[198:201], v[206:209], v[114:117]
	v_mfma_f32_16x16x32_bf16 v[102:105], v[190:193], v[216:219], v[102:105]
	v_mfma_f32_16x16x32_bf16 v[98:101], v[198:201], v[216:219], v[98:101]
	v_mfma_f32_16x16x32_bf16 v[86:89], v[190:193], v[224:227], v[86:89]
	v_mfma_f32_16x16x32_bf16 v[82:85], v[198:201], v[224:227], v[82:85]
	v_mfma_f32_16x16x32_bf16 v[70:73], v[190:193], v[232:235], v[70:73]
	v_mfma_f32_16x16x32_bf16 v[66:69], v[198:201], v[232:235], v[66:69]
	v_mfma_f32_16x16x32_bf16 v[118:121], v[194:197], v[212:215], v[118:121]
	v_mfma_f32_16x16x32_bf16 v[114:117], v[202:205], v[212:215], v[114:117]
	v_mfma_f32_16x16x32_bf16 v[102:105], v[194:197], v[220:223], v[102:105]
	v_mfma_f32_16x16x32_bf16 v[98:101], v[202:205], v[220:223], v[98:101]
	v_mfma_f32_16x16x32_bf16 v[86:89], v[194:197], v[228:231], v[86:89]
	v_mfma_f32_16x16x32_bf16 v[82:85], v[202:205], v[228:231], v[82:85]
	v_mfma_f32_16x16x32_bf16 v[70:73], v[194:197], v[236:239], v[70:73]
	v_mfma_f32_16x16x32_bf16 v[66:69], v[202:205], v[236:239], v[66:69]
	s_setprio 0
	s_barrier
	ds_read_b128 v[206:209], v176 offset:49152
	ds_read_b128 v[212:215], v176 offset:50176
	ds_read_b128 v[216:219], v176 offset:51200
	ds_read_b128 v[220:223], v176 offset:52224
	ds_read_b128 v[224:227], v176 offset:53248
	ds_read_b128 v[228:231], v176 offset:54272
	ds_read_b128 v[232:235], v176 offset:55296
	ds_read_b128 v[236:239], v176 offset:56320
	s_add_i32 s0, s33, s46
	v_lshl_add_u64 v[240:241], v[240:241], 0, s[26:27]
	s_mov_b32 m0, s0
	s_nop 0
	global_load_lds_dwordx4 v[240:241], off
	v_lshl_add_u64 v[240:241], v[242:243], 0, s[26:27]
	s_add_i32 m0, s0, 0x2000
	s_add_i32 s0, s76, s46
	global_load_lds_dwordx4 v[240:241], off
	v_lshl_add_u64 v[240:241], v[244:245], 0, s[26:27]
	s_mov_b32 m0, s0
	s_nop 0
	global_load_lds_dwordx4 v[240:241], off
	v_lshl_add_u64 v[240:241], v[246:247], 0, s[26:27]
	s_add_i32 m0, s0, 0x2000
	s_nop 0
	global_load_lds_dwordx4 v[240:241], off
	v_lshl_add_u64 v[240:241], v[248:249], 0, s[26:27]
	s_mov_b32 m0, s52
	s_nop 0
	global_load_lds_dwordx4 v[240:241], off
	v_lshl_add_u64 v[240:241], v[250:251], 0, s[26:27]
	s_mov_b32 m0, s53
	s_nop 0
	global_load_lds_dwordx4 v[240:241], off
	s_waitcnt vmcnt(6)
	s_waitcnt lgkmcnt(0)
	s_barrier
	s_setprio 1
	s_waitcnt lgkmcnt(0)
	v_mfma_f32_16x16x32_bf16 v[62:65], v[168:171], v[206:209], v[62:65]
	v_mfma_f32_16x16x32_bf16 v[58:61], v[182:185], v[206:209], v[58:61]
	v_mfma_f32_16x16x32_bf16 v[46:49], v[168:171], v[216:219], v[46:49]
	v_mfma_f32_16x16x32_bf16 v[42:45], v[182:185], v[216:219], v[42:45]
	v_mfma_f32_16x16x32_bf16 v[30:33], v[168:171], v[224:227], v[30:33]
	v_mfma_f32_16x16x32_bf16 v[26:29], v[182:185], v[224:227], v[26:29]
	v_mfma_f32_16x16x32_bf16 v[14:17], v[168:171], v[232:235], v[14:17]
	v_mfma_f32_16x16x32_bf16 v[10:13], v[182:185], v[232:235], v[10:13]
	v_mfma_f32_16x16x32_bf16 v[62:65], v[178:181], v[212:215], v[62:65]
	v_mfma_f32_16x16x32_bf16 v[58:61], v[186:189], v[212:215], v[58:61]
	v_mfma_f32_16x16x32_bf16 v[46:49], v[178:181], v[220:223], v[46:49]
	v_mfma_f32_16x16x32_bf16 v[42:45], v[186:189], v[220:223], v[42:45]
	v_mfma_f32_16x16x32_bf16 v[30:33], v[178:181], v[228:231], v[30:33]
	v_mfma_f32_16x16x32_bf16 v[26:29], v[186:189], v[228:231], v[26:29]
	v_mfma_f32_16x16x32_bf16 v[14:17], v[178:181], v[236:239], v[14:17]
	v_mfma_f32_16x16x32_bf16 v[10:13], v[186:189], v[236:239], v[10:13]
	s_setprio 0
	s_setprio 1
	v_mfma_f32_16x16x32_bf16 v[54:57], v[190:193], v[206:209], v[54:57]
	v_mfma_f32_16x16x32_bf16 v[50:53], v[198:201], v[206:209], v[50:53]
	v_mfma_f32_16x16x32_bf16 v[38:41], v[190:193], v[216:219], v[38:41]
	v_mfma_f32_16x16x32_bf16 v[34:37], v[198:201], v[216:219], v[34:37]
	v_mfma_f32_16x16x32_bf16 v[22:25], v[190:193], v[224:227], v[22:25]
	v_mfma_f32_16x16x32_bf16 v[18:21], v[198:201], v[224:227], v[18:21]
	v_mfma_f32_16x16x32_bf16 v[6:9], v[190:193], v[232:235], v[6:9]
	v_mfma_f32_16x16x32_bf16 v[2:5], v[198:201], v[232:235], v[2:5]
	v_mfma_f32_16x16x32_bf16 v[54:57], v[194:197], v[212:215], v[54:57]
	v_mfma_f32_16x16x32_bf16 v[50:53], v[202:205], v[212:215], v[50:53]
	v_mfma_f32_16x16x32_bf16 v[38:41], v[194:197], v[220:223], v[38:41]
	v_mfma_f32_16x16x32_bf16 v[34:37], v[202:205], v[220:223], v[34:37]
	v_mfma_f32_16x16x32_bf16 v[22:25], v[194:197], v[228:231], v[22:25]
	v_mfma_f32_16x16x32_bf16 v[18:21], v[202:205], v[228:231], v[18:21]
	v_mfma_f32_16x16x32_bf16 v[6:9], v[194:197], v[236:239], v[6:9]
	v_mfma_f32_16x16x32_bf16 v[2:5], v[202:205], v[236:239], v[2:5]
	s_setprio 0
	s_barrier
	s_add_u32 s40, s40, 0x100
	s_addc_u32 s41, s41, 0
	s_cmp_ge_i32 s75, s54
	s_cbranch_scc0 .LBB0_982

; #define PG8_STAGE(bufoff, gbase, voff) do { _Pragma("unroll") for (int _i = 0; _i < 2; ++_i) \
;         __builtin_amdgcn_global_load_lds((const unsigned*)((const char*)(gbase) + (voff)[_i]), (PG8_LAS unsigned*)(lds + (bufoff) + ldsw + _i * 8192), 16, 0, 0); } while (0)
; #define PG8_LDA(dst, b, h) do { _Pragma("unroll") for (int m = 0; m < 4; ++m) { const bf16x8 f0_ = *(const PG8_LAS bf16x8*)(lds + PG8_SA(b, h) + aoff + m * 2048), f1_ = *(const PG8_LAS bf16x8*)(lds + PG8_SA(b, h) + aoff + m * 2048 + 1024); dst[m].set(f0_, f1_); } } while (0)
; #define PG8_LDB(dst, b, h) do { _Pragma("unroll") for (int n = 0; n < 2; ++n) { const bf16x8 f0_ = *(const PG8_LAS bf16x8*)(lds + PG8_SB(b, h) + boff + n * 2048), f1_ = *(const PG8_LAS bf16x8*)(lds + PG8_SB(b, h) + boff + n * 2048 + 1024); dst[n].set(f0_, f1_); } } while (0)
; #define PG8_WAIT_V(n) asm volatile("s_waitcnt vmcnt(" #n ")" ::: "memory")
; #define PG8_WAIT_L(n) asm volatile("s_waitcnt lgkmcnt(" #n ")" ::: "memory")
; #define PG8_BAR __builtin_amdgcn_s_barrier()
; #define PG8_SCHED __builtin_amdgcn_sched_barrier(0)
; template <class Epi, class Sched, bool ALIGN_EPI = false, bool SP2 = false>
; __device__ __forceinline__ void gemm_phase(PG8_LAS unsigned char* lds, const Gemm g, const Sched& S, const Epi& E) {
;     ...
;             const bool last = (t == nt - 2);
;             const char* a1 = cA + (size_t)(t + 1) * kstep;
;             const char* a2 = last ? nA : cA + (size_t)(t + 2) * kstep; const char* b2 = last ? nB : cB + (size_t)(t + 2) * kstep;
;             const char* a3 = a2 + kstep; const char* b3 = b2 + kstep;
;             if (last && has_next) S.a_ready(nxt);
;             if constexpr (SP2) {
;             PG8_LDB(B0, 0, 0); PG8_LDB(B1, 0, 1); PG8_SCHED; PG8_LDA(At, 0, 0); PG8_STAGE(PG8_SA(1, 1), a1 + hstep, voffA);
;             PG8_WAIT_V(8); PG8_WAIT_L(0); PG8_BAR; PG8_MMA(0, 0, At, B0); PG8_MMA(0, 1, At, B1); PG8_BAR; PG8_SCHED;
;             PG8_LDA(At, 0, 1); PG8_STAGE(PG8_SB(0, 0), b2, voffB); PG8_STAGE(PG8_SB(0, 1), b2 + hstepB, voffB); PG8_STAGE(PG8_SA(0, 0), a2, voffA);
;             PG8_WAIT_V(8); PG8_WAIT_L(0); PG8_BAR; PG8_MMA(1, 0, At, B0); PG8_MMA(1, 1, At, B1); PG8_BAR; PG8_SCHED;
.LBB0_1070:
	ds_read_b128 v[130:133], v193
	ds_read_b128 v[134:137], v193 offset:1024
	ds_read_b128 v[138:141], v193 offset:2048
	ds_read_b128 v[142:145], v193 offset:3072
	ds_read_b128 v[146:149], v194
	ds_read_b128 v[150:153], v194 offset:1024
	ds_read_b128 v[154:157], v194 offset:2048
	ds_read_b128 v[158:161], v194 offset:3072
	ds_read_b128 v[162:165], v195
	ds_read_b128 v[186:189], v195 offset:1024
	ds_read_b128 v[198:201], v195 offset:2048
	ds_read_b128 v[202:205], v195 offset:3072
	ds_read_b128 v[206:209], v195 offset:4096
	ds_read_b128 v[212:215], v195 offset:5120
	ds_read_b128 v[216:219], v195 offset:6144
	ds_read_b128 v[220:223], v195 offset:7168
	s_add_i32 s95, s58, 2
	s_add_u32 s0, s56, 0x80
	s_addc_u32 s1, s57, 0
	s_cmp_eq_u32 s78, s58
	s_cselect_b32 s58, s2, s0
	s_cselect_b32 s59, s3, s1
	s_cselect_b32 s1, s55, s94
	s_cselect_b32 s0, s54, s93
	s_cmp_eq_u32 s99, 0
	s_cbranch_scc1 .Lkr2_a
	v_lshl_add_u64 v[232:233], v[232:233], 0, s[28:29]
	s_mov_b32 m0, s74
	v_lshl_add_u64 v[234:235], v[234:235], 0, s[28:29]
	global_load_lds_dwordx4 v[232:233], off
	s_mov_b32 m0, s75
	s_nop 0
	global_load_lds_dwordx4 v[234:235], off
.Lkr2_a:
	v_lshl_add_u64 v[224:225], s[56:57], 0, v[176:177]
	s_add_i32 m0, s67, 0xc000
	s_nop 0
	global_load_lds_dwordx4 v[224:225], off
	v_lshl_add_u64 v[224:225], s[56:57], 0, v[178:179]
	s_add_i32 m0, s67, 0xe000
	s_nop 0
	global_load_lds_dwordx4 v[224:225], off
	s_waitcnt vmcnt(8)
	s_waitcnt lgkmcnt(0)
	s_barrier
	s_setprio 1
	s_waitcnt lgkmcnt(0)
	v_mfma_f32_16x16x32_bf16 v[126:129], v[130:133], v[162:165], v[126:129]
	v_mfma_f32_16x16x32_bf16 v[122:125], v[138:141], v[162:165], v[122:125]
	v_mfma_f32_16x16x32_bf16 v[58:61], v[130:133], v[198:201], v[58:61]
	v_mfma_f32_16x16x32_bf16 v[62:65], v[138:141], v[198:201], v[62:65]
	v_mfma_f32_16x16x32_bf16 v[106:109], v[130:133], v[206:209], v[106:109]
	v_mfma_f32_16x16x32_bf16 v[110:113], v[138:141], v[206:209], v[110:113]
	v_mfma_f32_16x16x32_bf16 v[98:101], v[130:133], v[216:219], v[98:101]
	v_mfma_f32_16x16x32_bf16 v[102:105], v[138:141], v[216:219], v[102:105]
	v_mfma_f32_16x16x32_bf16 v[126:129], v[134:137], v[186:189], v[126:129]
	v_mfma_f32_16x16x32_bf16 v[122:125], v[142:145], v[186:189], v[122:125]
	v_mfma_f32_16x16x32_bf16 v[58:61], v[134:137], v[202:205], v[58:61]
	v_mfma_f32_16x16x32_bf16 v[62:65], v[142:145], v[202:205], v[62:65]
	v_mfma_f32_16x16x32_bf16 v[106:109], v[134:137], v[212:215], v[106:109]
	v_mfma_f32_16x16x32_bf16 v[110:113], v[142:145], v[212:215], v[110:113]
	v_mfma_f32_16x16x32_bf16 v[98:101], v[134:137], v[220:223], v[98:101]
	v_mfma_f32_16x16x32_bf16 v[102:105], v[142:145], v[220:223], v[102:105]
	s_setprio 0
	s_setprio 1
	v_mfma_f32_16x16x32_bf16 v[118:121], v[146:149], v[162:165], v[118:121]
	v_mfma_f32_16x16x32_bf16 v[114:117], v[154:157], v[162:165], v[114:117]
	v_mfma_f32_16x16x32_bf16 v[50:53], v[146:149], v[198:201], v[50:53]
	v_mfma_f32_16x16x32_bf16 v[54:57], v[154:157], v[198:201], v[54:57]
	v_mfma_f32_16x16x32_bf16 v[90:93], v[146:149], v[206:209], v[90:93]
	v_mfma_f32_16x16x32_bf16 v[94:97], v[154:157], v[206:209], v[94:97]
	v_mfma_f32_16x16x32_bf16 v[74:77], v[146:149], v[216:219], v[74:77]
	v_mfma_f32_16x16x32_bf16 v[78:81], v[154:157], v[216:219], v[78:81]
	v_mfma_f32_16x16x32_bf16 v[118:121], v[150:153], v[186:189], v[118:121]
	v_mfma_f32_16x16x32_bf16 v[114:117], v[158:161], v[186:189], v[114:117]
	v_mfma_f32_16x16x32_bf16 v[50:53], v[150:153], v[202:205], v[50:53]
	v_mfma_f32_16x16x32_bf16 v[54:57], v[158:161], v[202:205], v[54:57]
	v_mfma_f32_16x16x32_bf16 v[90:93], v[150:153], v[212:215], v[90:93]
	v_mfma_f32_16x16x32_bf16 v[94:97], v[158:161], v[212:215], v[94:97]
	v_mfma_f32_16x16x32_bf16 v[74:77], v[150:153], v[220:223], v[74:77]
	v_mfma_f32_16x16x32_bf16 v[78:81], v[158:161], v[220:223], v[78:81]
	s_setprio 0
	s_barrier
	ds_read_b128 v[162:165], v195 offset:16384
	ds_read_b128 v[186:189], v195 offset:17408
	ds_read_b128 v[198:201], v195 offset:18432
	ds_read_b128 v[202:205], v195 offset:19456
	ds_read_b128 v[206:209], v195 offset:20480
	ds_read_b128 v[212:215], v195 offset:21504
	ds_read_b128 v[216:219], v195 offset:22528
	ds_read_b128 v[220:223], v195 offset:23552
	s_add_i32 s33, s82, s66
	v_lshl_add_u64 v[224:225], s[0:1], 0, v[168:169]
	s_mov_b32 m0, s33
	s_nop 0
	global_load_lds_dwordx4 v[224:225], off
	s_add_i32 m0, s33, 0x2000
	v_lshl_add_u64 v[226:227], s[0:1], 0, v[172:173]
	s_add_u32 s0, s0, s16
	s_addc_u32 s1, s1, s17
	s_add_i32 s33, s83, s66
	global_load_lds_dwordx4 v[226:227], off
	v_lshl_add_u64 v[228:229], s[0:1], 0, v[168:169]
	s_mov_b32 m0, s33
	v_lshl_add_u64 v[230:231], s[0:1], 0, v[172:173]
	global_load_lds_dwordx4 v[228:229], off
	s_add_i32 m0, s33, 0x2000
	v_lshl_add_u64 v[232:233], s[58:59], 0, v[166:167]
	global_load_lds_dwordx4 v[230:231], off
	v_lshl_add_u64 v[234:235], s[58:59], 0, v[170:171]
	s_waitcnt vmcnt(6)
	s_waitcnt lgkmcnt(0)
	s_barrier
; #define PG8_STAGE(bufoff, gbase, voff) do { _Pragma("unroll") for (int _i = 0; _i < 2; ++_i) \
;         __builtin_amdgcn_global_load_lds((const unsigned*)((const char*)(gbase) + (voff)[_i]), (PG8_LAS unsigned*)(lds + (bufoff) + ldsw + _i * 8192), 16, 0, 0); } while (0)
; #define PG8_LDA(dst, b, h) do { _Pragma("unroll") for (int m = 0; m < 4; ++m) { const bf16x8 f0_ = *(const PG8_LAS bf16x8*)(lds + PG8_SA(b, h) + aoff + m * 2048), f1_ = *(const PG8_LAS bf16x8*)(lds + PG8_SA(b, h) + aoff + m * 2048 + 1024); dst[m].set(f0_, f1_); } } while (0)
; #define PG8_LDB(dst, b, h) do { _Pragma("unroll") for (int n = 0; n < 2; ++n) { const bf16x8 f0_ = *(const PG8_LAS bf16x8*)(lds + PG8_SB(b, h) + boff + n * 2048), f1_ = *(const PG8_LAS bf16x8*)(lds + PG8_SB(b, h) + boff + n * 2048 + 1024); dst[n].set(f0_, f1_); } } while (0)
; #define PG8_WAIT_V(n) asm volatile("s_waitcnt vmcnt(" #n ")" ::: "memory")
; #define PG8_WAIT_L(n) asm volatile("s_waitcnt lgkmcnt(" #n ")" ::: "memory")
; #define PG8_BAR __builtin_amdgcn_s_barrier()
; #define PG8_SCHED __builtin_amdgcn_sched_barrier(0)
; template <class Epi, class Sched, bool ALIGN_EPI = false, bool SP2 = false>
; __device__ __forceinline__ void gemm_phase(PG8_LAS unsigned char* lds, const Gemm g, const Sched& S, const Epi& E) {
;     ...
;             PG8_WAIT_V(8); PG8_WAIT_L(0); PG8_BAR; PG8_MMA(1, 0, At, B0); PG8_MMA(1, 1, At, B1); PG8_BAR; PG8_SCHED;
;             PG8_LDB(B0, 1, 0); PG8_LDB(B1, 1, 1); PG8_SCHED; PG8_LDA(At, 1, 0); PG8_STAGE(PG8_SA(0, 1), a2 + hstep, voffA);
;             PG8_WAIT_V(8); PG8_WAIT_L(0); PG8_BAR; PG8_MMA(0, 0, At, B0); PG8_MMA(0, 1, At, B1); PG8_BAR; PG8_SCHED;
	s_setprio 1
	s_waitcnt lgkmcnt(0)
	v_mfma_f32_16x16x32_bf16 v[82:85], v[130:133], v[162:165], v[82:85]
	v_mfma_f32_16x16x32_bf16 v[86:89], v[138:141], v[162:165], v[86:89]
	v_mfma_f32_16x16x32_bf16 v[46:49], v[130:133], v[198:201], v[46:49]
	v_mfma_f32_16x16x32_bf16 v[42:45], v[138:141], v[198:201], v[42:45]
	v_mfma_f32_16x16x32_bf16 v[30:33], v[130:133], v[206:209], v[30:33]
	v_mfma_f32_16x16x32_bf16 v[26:29], v[138:141], v[206:209], v[26:29]
	v_mfma_f32_16x16x32_bf16 v[14:17], v[130:133], v[216:219], v[14:17]
	v_mfma_f32_16x16x32_bf16 v[6:9], v[138:141], v[216:219], v[6:9]
	v_mfma_f32_16x16x32_bf16 v[82:85], v[134:137], v[186:189], v[82:85]
	v_mfma_f32_16x16x32_bf16 v[86:89], v[142:145], v[186:189], v[86:89]
	v_mfma_f32_16x16x32_bf16 v[46:49], v[134:137], v[202:205], v[46:49]
	v_mfma_f32_16x16x32_bf16 v[42:45], v[142:145], v[202:205], v[42:45]
	v_mfma_f32_16x16x32_bf16 v[30:33], v[134:137], v[212:215], v[30:33]
	v_mfma_f32_16x16x32_bf16 v[26:29], v[142:145], v[212:215], v[26:29]
	v_mfma_f32_16x16x32_bf16 v[14:17], v[134:137], v[220:223], v[14:17]
	v_mfma_f32_16x16x32_bf16 v[6:9], v[142:145], v[220:223], v[6:9]
	s_setprio 0
	s_setprio 1
	v_mfma_f32_16x16x32_bf16 v[66:69], v[146:149], v[162:165], v[66:69]
	v_mfma_f32_16x16x32_bf16 v[70:73], v[154:157], v[162:165], v[70:73]
	v_mfma_f32_16x16x32_bf16 v[38:41], v[146:149], v[198:201], v[38:41]
	v_mfma_f32_16x16x32_bf16 v[34:37], v[154:157], v[198:201], v[34:37]
	v_mfma_f32_16x16x32_bf16 v[22:25], v[146:149], v[206:209], v[22:25]
	v_mfma_f32_16x16x32_bf16 v[18:21], v[154:157], v[206:209], v[18:21]
	v_mfma_f32_16x16x32_bf16 v[10:13], v[146:149], v[216:219], v[10:13]
	v_mfma_f32_16x16x32_bf16 v[2:5], v[154:157], v[216:219], v[2:5]
	v_mfma_f32_16x16x32_bf16 v[66:69], v[150:153], v[186:189], v[66:69]
	v_mfma_f32_16x16x32_bf16 v[70:73], v[158:161], v[186:189], v[70:73]
	v_mfma_f32_16x16x32_bf16 v[38:41], v[150:153], v[202:205], v[38:41]
	v_mfma_f32_16x16x32_bf16 v[34:37], v[158:161], v[202:205], v[34:37]
	v_mfma_f32_16x16x32_bf16 v[22:25], v[150:153], v[212:215], v[22:25]
	v_mfma_f32_16x16x32_bf16 v[18:21], v[158:161], v[212:215], v[18:21]
	v_mfma_f32_16x16x32_bf16 v[10:13], v[150:153], v[220:223], v[10:13]
	v_mfma_f32_16x16x32_bf16 v[2:5], v[158:161], v[220:223], v[2:5]
	s_setprio 0
	s_barrier
	ds_read_b128 v[162:165], v195 offset:32768
	ds_read_b128 v[186:189], v195 offset:33792
	ds_read_b128 v[198:201], v195 offset:34816
	ds_read_b128 v[202:205], v195 offset:35840
	ds_read_b128 v[206:209], v195 offset:36864
	ds_read_b128 v[212:215], v195 offset:37888
	ds_read_b128 v[216:219], v195 offset:38912
	ds_read_b128 v[220:223], v195 offset:39936
	s_add_i32 s33, 0, 0x18000
	s_add_i32 s96, 0, 0x1c000
	v_add_u32_e32 v142, s33, v190
	v_add_u32_e32 v158, s96, v190
	ds_read_b128 v[130:133], v142
	ds_read_b128 v[134:137], v142 offset:1024
	ds_read_b128 v[138:141], v142 offset:2048
	ds_read_b128 v[142:145], v142 offset:3072
	ds_read_b128 v[146:149], v158
	ds_read_b128 v[150:153], v158 offset:1024
	ds_read_b128 v[154:157], v158 offset:2048
	ds_read_b128 v[158:161], v158 offset:3072
	s_add_u32 s0, s58, s14
	s_addc_u32 s1, s59, s15
	s_mov_b32 m0, s71
	v_lshl_add_u64 v[236:237], s[0:1], 0, v[166:167]
	s_mov_b32 m0, s67
	s_nop 0
	global_load_lds_dwordx4 v[232:233], off
	s_mov_b32 m0, s69
	s_nop 0
	global_load_lds_dwordx4 v[234:235], off
	s_mov_b32 m0, s71
	s_nop 0
	global_load_lds_dwordx4 v[236:237], off
	v_lshl_add_u64 v[236:237], s[0:1], 0, v[170:171]
	s_mov_b32 m0, s73
	s_nop 0
	global_load_lds_dwordx4 v[236:237], off
	s_waitcnt vmcnt(8)
	s_waitcnt lgkmcnt(0)
	s_barrier
; #define PG8_STAGE(bufoff, gbase, voff) do { _Pragma("unroll") for (int _i = 0; _i < 2; ++_i) \
;         __builtin_amdgcn_global_load_lds((const unsigned*)((const char*)(gbase) + (voff)[_i]), (PG8_LAS unsigned*)(lds + (bufoff) + ldsw + _i * 8192), 16, 0, 0); } while (0)
; #define PG8_LDA(dst, b, h) do { _Pragma("unroll") for (int m = 0; m < 4; ++m) { const bf16x8 f0_ = *(const PG8_LAS bf16x8*)(lds + PG8_SA(b, h) + aoff + m * 2048), f1_ = *(const PG8_LAS bf16x8*)(lds + PG8_SA(b, h) + aoff + m * 2048 + 1024); dst[m].set(f0_, f1_); } } while (0)
; #define PG8_WAIT_V(n) asm volatile("s_waitcnt vmcnt(" #n ")" ::: "memory")
; #define PG8_WAIT_L(n) asm volatile("s_waitcnt lgkmcnt(" #n ")" ::: "memory")
; #define PG8_BAR __builtin_amdgcn_s_barrier()
; #define PG8_SCHED __builtin_amdgcn_sched_barrier(0)
; template <class Epi, class Sched, bool ALIGN_EPI = false, bool SP2 = false>
; __device__ __forceinline__ void gemm_phase(PG8_LAS unsigned char* lds, const Gemm g, const Sched& S, const Epi& E) {
;     ...
;             PG8_WAIT_V(8); PG8_WAIT_L(0); PG8_BAR; PG8_MMA(0, 0, At, B0); PG8_MMA(0, 1, At, B1); PG8_BAR; PG8_SCHED;
;             PG8_LDA(At, 1, 1); PG8_STAGE(PG8_SB(1, 0), b3, voffB); PG8_STAGE(PG8_SB(1, 1), b3 + hstepB, voffB); PG8_STAGE(PG8_SA(1, 0), a3, voffA);
	s_setprio 1
	s_waitcnt lgkmcnt(0)
	v_mfma_f32_16x16x32_bf16 v[126:129], v[130:133], v[162:165], v[126:129]
	v_mfma_f32_16x16x32_bf16 v[122:125], v[138:141], v[162:165], v[122:125]
	v_mfma_f32_16x16x32_bf16 v[58:61], v[130:133], v[198:201], v[58:61]
	v_mfma_f32_16x16x32_bf16 v[62:65], v[138:141], v[198:201], v[62:65]
	v_mfma_f32_16x16x32_bf16 v[106:109], v[130:133], v[206:209], v[106:109]
	v_mfma_f32_16x16x32_bf16 v[110:113], v[138:141], v[206:209], v[110:113]
	v_mfma_f32_16x16x32_bf16 v[98:101], v[130:133], v[216:219], v[98:101]
	v_mfma_f32_16x16x32_bf16 v[102:105], v[138:141], v[216:219], v[102:105]
	v_mfma_f32_16x16x32_bf16 v[126:129], v[134:137], v[186:189], v[126:129]
	v_mfma_f32_16x16x32_bf16 v[122:125], v[142:145], v[186:189], v[122:125]
	v_mfma_f32_16x16x32_bf16 v[58:61], v[134:137], v[202:205], v[58:61]
	v_mfma_f32_16x16x32_bf16 v[62:65], v[142:145], v[202:205], v[62:65]
	v_mfma_f32_16x16x32_bf16 v[106:109], v[134:137], v[212:215], v[106:109]
	v_mfma_f32_16x16x32_bf16 v[110:113], v[142:145], v[212:215], v[110:113]
	v_mfma_f32_16x16x32_bf16 v[98:101], v[134:137], v[220:223], v[98:101]
	v_mfma_f32_16x16x32_bf16 v[102:105], v[142:145], v[220:223], v[102:105]
	s_setprio 0
	s_setprio 1
	v_mfma_f32_16x16x32_bf16 v[118:121], v[146:149], v[162:165], v[118:121]
	v_mfma_f32_16x16x32_bf16 v[114:117], v[154:157], v[162:165], v[114:117]
	v_mfma_f32_16x16x32_bf16 v[50:53], v[146:149], v[198:201], v[50:53]
	v_mfma_f32_16x16x32_bf16 v[54:57], v[154:157], v[198:201], v[54:57]
	v_mfma_f32_16x16x32_bf16 v[90:93], v[146:149], v[206:209], v[90:93]
	v_mfma_f32_16x16x32_bf16 v[94:97], v[154:157], v[206:209], v[94:97]
	v_mfma_f32_16x16x32_bf16 v[74:77], v[146:149], v[216:219], v[74:77]
	v_mfma_f32_16x16x32_bf16 v[78:81], v[154:157], v[216:219], v[78:81]
	v_mfma_f32_16x16x32_bf16 v[118:121], v[150:153], v[186:189], v[118:121]
	v_mfma_f32_16x16x32_bf16 v[114:117], v[158:161], v[186:189], v[114:117]
	v_mfma_f32_16x16x32_bf16 v[50:53], v[150:153], v[202:205], v[50:53]
	v_mfma_f32_16x16x32_bf16 v[54:57], v[158:161], v[202:205], v[54:57]
	v_mfma_f32_16x16x32_bf16 v[90:93], v[150:153], v[212:215], v[90:93]
	v_mfma_f32_16x16x32_bf16 v[94:97], v[158:161], v[212:215], v[94:97]
	v_mfma_f32_16x16x32_bf16 v[74:77], v[150:153], v[220:223], v[74:77]
	v_mfma_f32_16x16x32_bf16 v[78:81], v[158:161], v[220:223], v[78:81]
	s_setprio 0
	s_barrier
	ds_read_b128 v[162:165], v195 offset:49152
	ds_read_b128 v[186:189], v195 offset:50176
	ds_read_b128 v[198:201], v195 offset:51200
	ds_read_b128 v[202:205], v195 offset:52224
	ds_read_b128 v[206:209], v195 offset:53248
	ds_read_b128 v[212:215], v195 offset:54272
	ds_read_b128 v[216:219], v195 offset:55296
	ds_read_b128 v[220:223], v195 offset:56320
	s_add_i32 s0, s33, s66
	v_lshl_add_u64 v[224:225], v[224:225], 0, s[28:29]
	s_mov_b32 m0, s0
	s_nop 0
	global_load_lds_dwordx4 v[224:225], off
	v_lshl_add_u64 v[224:225], v[226:227], 0, s[28:29]
	s_add_i32 m0, s0, 0x2000
	s_add_i32 s0, s96, s66
	global_load_lds_dwordx4 v[224:225], off
	v_lshl_add_u64 v[224:225], v[228:229], 0, s[28:29]
	s_mov_b32 m0, s0
	s_nop 0
	global_load_lds_dwordx4 v[224:225], off
	v_lshl_add_u64 v[224:225], v[230:231], 0, s[28:29]
	s_add_i32 m0, s0, 0x2000
	s_nop 0
	global_load_lds_dwordx4 v[224:225], off
	s_cmp_ge_i32 s95, s76
	s_cbranch_scc0 .Lkr2_b
	v_lshl_add_u64 v[224:225], v[232:233], 0, s[28:29]
	s_mov_b32 m0, s74
	s_nop 0
	global_load_lds_dwordx4 v[224:225], off
	v_lshl_add_u64 v[224:225], v[234:235], 0, s[28:29]
	s_mov_b32 m0, s75
	s_nop 0
	global_load_lds_dwordx4 v[224:225], off

; #define PG8_STAGE(bufoff, gbase, voff) do { _Pragma("unroll") for (int _i = 0; _i < 2; ++_i) \
;         __builtin_amdgcn_global_load_lds((const unsigned*)((const char*)(gbase) + (voff)[_i]), (PG8_LAS unsigned*)(lds + (bufoff) + ldsw + _i * 8192), 16, 0, 0); } while (0)
; #define PG8_LDA(dst, b, h) do { _Pragma("unroll") for (int m = 0; m < 4; ++m) { const bf16x8 f0_ = *(const PG8_LAS bf16x8*)(lds + PG8_SA(b, h) + aoff + m * 2048), f1_ = *(const PG8_LAS bf16x8*)(lds + PG8_SA(b, h) + aoff + m * 2048 + 1024); dst[m].set(f0_, f1_); } } while (0)
; #define PG8_LDB(dst, b, h) do { _Pragma("unroll") for (int n = 0; n < 2; ++n) { const bf16x8 f0_ = *(const PG8_LAS bf16x8*)(lds + PG8_SB(b, h) + boff + n * 2048), f1_ = *(const PG8_LAS bf16x8*)(lds + PG8_SB(b, h) + boff + n * 2048 + 1024); dst[n].set(f0_, f1_); } } while (0)
; #define PG8_WAIT_V(n) asm volatile("s_waitcnt vmcnt(" #n ")" ::: "memory")
; #define PG8_WAIT_L(n) asm volatile("s_waitcnt lgkmcnt(" #n ")" ::: "memory")
; #define PG8_BAR __builtin_amdgcn_s_barrier()
; #define PG8_SCHED __builtin_amdgcn_sched_barrier(0)
; template <class Epi, class Sched, bool ALIGN_EPI = false, bool SP2 = false>
; __device__ __forceinline__ void gemm_phase(PG8_LAS unsigned char* lds, const Gemm g, const Sched& S, const Epi& E) {
;     ...
;             const bool last = (t == nt - 2);
;             const char* a1 = cA + (size_t)(t + 1) * kstep;
;             const char* a2 = last ? nA : cA + (size_t)(t + 2) * kstep; const char* b2 = last ? nB : cB + (size_t)(t + 2) * kstep;
;             const char* a3 = a2 + kstep; const char* b3 = b2 + kstep;
;             if (last && has_next) S.a_ready(nxt);
;             if constexpr (SP2) {
;             PG8_LDB(B0, 0, 0); PG8_LDB(B1, 0, 1); PG8_SCHED; PG8_LDA(At, 0, 0); PG8_STAGE(PG8_SA(1, 1), a1 + hstep, voffA);
;             PG8_WAIT_V(8); PG8_WAIT_L(0); PG8_BAR; PG8_MMA(0, 0, At, B0); PG8_MMA(0, 1, At, B1); PG8_BAR; PG8_SCHED;
;             PG8_LDA(At, 0, 1); PG8_STAGE(PG8_SB(0, 0), b2, voffB); PG8_STAGE(PG8_SB(0, 1), b2 + hstepB, voffB); PG8_STAGE(PG8_SA(0, 0), a2, voffA);
;             PG8_WAIT_V(8); PG8_WAIT_L(0); PG8_BAR; PG8_MMA(1, 0, At, B0); PG8_MMA(1, 1, At, B1); PG8_BAR; PG8_SCHED;
.LBB0_1171:
	ds_read_b128 v[156:159], v152
	ds_read_b128 v[160:163], v152 offset:1024
	ds_read_b128 v[164:167], v152 offset:2048
	ds_read_b128 v[168:171], v152 offset:3072
	ds_read_b128 v[172:175], v153
	ds_read_b128 v[176:179], v153 offset:1024
	ds_read_b128 v[180:183], v153 offset:2048
	ds_read_b128 v[184:187], v153 offset:3072
	ds_read_b128 v[188:191], v154
	ds_read_b128 v[192:195], v154 offset:1024
	ds_read_b128 v[196:199], v154 offset:2048
	ds_read_b128 v[200:203], v154 offset:3072
	ds_read_b128 v[204:207], v154 offset:4096
	ds_read_b128 v[212:215], v154 offset:5120
	ds_read_b128 v[216:219], v154 offset:6144
	ds_read_b128 v[220:223], v154 offset:7168
	s_add_i32 s61, s34, 2
	s_add_u32 s0, s30, 0x80
	s_addc_u32 s1, s31, 0
	s_cmp_eq_u32 s49, s34
	s_cselect_b32 s34, s6, s0
	s_cselect_b32 s35, s7, s1
	s_cselect_b32 s1, s29, s59
	s_cselect_b32 s0, s28, s58
	s_cmp_eq_u32 s99, 0
	s_cbranch_scc1 .Lkr3_a
	v_lshl_add_u64 v[228:229], v[228:229], 0, s[22:23]
	s_mov_b32 m0, s45
	v_lshl_add_u64 v[230:231], v[230:231], 0, s[22:23]
	global_load_lds_dwordx4 v[228:229], off
	s_mov_b32 m0, s46
	s_nop 0
	global_load_lds_dwordx4 v[230:231], off
.Lkr3_a:
	v_lshl_add_u64 v[148:149], s[30:31], 0, v[140:141]
	s_add_i32 m0, s40, 0xc000
	s_nop 0
	global_load_lds_dwordx4 v[148:149], off
	v_lshl_add_u64 v[148:149], s[30:31], 0, v[142:143]
	s_add_i32 m0, s40, 0xe000
	s_nop 0
	global_load_lds_dwordx4 v[148:149], off
	s_waitcnt vmcnt(8)
	s_waitcnt lgkmcnt(0)
	s_barrier
	s_setprio 1
	s_waitcnt lgkmcnt(0)
	v_mfma_f32_16x16x32_bf16 v[126:129], v[156:159], v[188:191], v[126:129]
	v_mfma_f32_16x16x32_bf16 v[122:125], v[164:167], v[188:191], v[122:125]
	v_mfma_f32_16x16x32_bf16 v[110:113], v[156:159], v[196:199], v[110:113]
	v_mfma_f32_16x16x32_bf16 v[106:109], v[164:167], v[196:199], v[106:109]
	v_mfma_f32_16x16x32_bf16 v[94:97], v[156:159], v[204:207], v[94:97]
	v_mfma_f32_16x16x32_bf16 v[90:93], v[164:167], v[204:207], v[90:93]
	v_mfma_f32_16x16x32_bf16 v[78:81], v[156:159], v[216:219], v[78:81]
	v_mfma_f32_16x16x32_bf16 v[74:77], v[164:167], v[216:219], v[74:77]
	v_mfma_f32_16x16x32_bf16 v[126:129], v[160:163], v[192:195], v[126:129]
	v_mfma_f32_16x16x32_bf16 v[122:125], v[168:171], v[192:195], v[122:125]
	v_mfma_f32_16x16x32_bf16 v[110:113], v[160:163], v[200:203], v[110:113]
	v_mfma_f32_16x16x32_bf16 v[106:109], v[168:171], v[200:203], v[106:109]
	v_mfma_f32_16x16x32_bf16 v[94:97], v[160:163], v[212:215], v[94:97]
	v_mfma_f32_16x16x32_bf16 v[90:93], v[168:171], v[212:215], v[90:93]
	v_mfma_f32_16x16x32_bf16 v[78:81], v[160:163], v[220:223], v[78:81]
	v_mfma_f32_16x16x32_bf16 v[74:77], v[168:171], v[220:223], v[74:77]
	s_setprio 0
	s_setprio 1
	v_mfma_f32_16x16x32_bf16 v[118:121], v[172:175], v[188:191], v[118:121]
	v_mfma_f32_16x16x32_bf16 v[114:117], v[180:183], v[188:191], v[114:117]
	v_mfma_f32_16x16x32_bf16 v[102:105], v[172:175], v[196:199], v[102:105]
	v_mfma_f32_16x16x32_bf16 v[98:101], v[180:183], v[196:199], v[98:101]
	v_mfma_f32_16x16x32_bf16 v[86:89], v[172:175], v[204:207], v[86:89]
	v_mfma_f32_16x16x32_bf16 v[82:85], v[180:183], v[204:207], v[82:85]
	v_mfma_f32_16x16x32_bf16 v[70:73], v[172:175], v[216:219], v[70:73]
	v_mfma_f32_16x16x32_bf16 v[66:69], v[180:183], v[216:219], v[66:69]
	v_mfma_f32_16x16x32_bf16 v[118:121], v[176:179], v[192:195], v[118:121]
	v_mfma_f32_16x16x32_bf16 v[114:117], v[184:187], v[192:195], v[114:117]
	v_mfma_f32_16x16x32_bf16 v[102:105], v[176:179], v[200:203], v[102:105]
	v_mfma_f32_16x16x32_bf16 v[98:101], v[184:187], v[200:203], v[98:101]
	v_mfma_f32_16x16x32_bf16 v[86:89], v[176:179], v[212:215], v[86:89]
	v_mfma_f32_16x16x32_bf16 v[82:85], v[184:187], v[212:215], v[82:85]
	v_mfma_f32_16x16x32_bf16 v[70:73], v[176:179], v[220:223], v[70:73]
	v_mfma_f32_16x16x32_bf16 v[66:69], v[184:187], v[220:223], v[66:69]
	s_setprio 0
	s_barrier
	ds_read_b128 v[188:191], v154 offset:16384
	ds_read_b128 v[192:195], v154 offset:17408
	ds_read_b128 v[196:199], v154 offset:18432
	ds_read_b128 v[200:203], v154 offset:19456
	ds_read_b128 v[204:207], v154 offset:20480
	ds_read_b128 v[212:215], v154 offset:21504
	ds_read_b128 v[216:219], v154 offset:22528
	ds_read_b128 v[220:223], v154 offset:23552
	s_add_i32 s33, s52, s39
	v_lshl_add_u64 v[148:149], s[0:1], 0, v[132:133]
	s_mov_b32 m0, s33
	s_nop 0
	global_load_lds_dwordx4 v[148:149], off
	s_add_i32 m0, s33, 0x2000
	v_lshl_add_u64 v[208:209], s[0:1], 0, v[136:137]
	s_add_u32 s0, s0, s14
	s_addc_u32 s1, s1, s15
	s_add_i32 s33, s53, s39
	global_load_lds_dwordx4 v[208:209], off
	v_lshl_add_u64 v[224:225], s[0:1], 0, v[132:133]
	s_mov_b32 m0, s33
	v_lshl_add_u64 v[226:227], s[0:1], 0, v[136:137]
	global_load_lds_dwordx4 v[224:225], off
	s_add_i32 m0, s33, 0x2000
	v_lshl_add_u64 v[228:229], s[34:35], 0, v[130:131]
	global_load_lds_dwordx4 v[226:227], off
	v_lshl_add_u64 v[230:231], s[34:35], 0, v[134:135]
	s_waitcnt vmcnt(6)
	s_waitcnt lgkmcnt(0)
	s_barrier
; #define PG8_STAGE(bufoff, gbase, voff) do { _Pragma("unroll") for (int _i = 0; _i < 2; ++_i) \
;         __builtin_amdgcn_global_load_lds((const unsigned*)((const char*)(gbase) + (voff)[_i]), (PG8_LAS unsigned*)(lds + (bufoff) + ldsw + _i * 8192), 16, 0, 0); } while (0)
; #define PG8_LDA(dst, b, h) do { _Pragma("unroll") for (int m = 0; m < 4; ++m) { const bf16x8 f0_ = *(const PG8_LAS bf16x8*)(lds + PG8_SA(b, h) + aoff + m * 2048), f1_ = *(const PG8_LAS bf16x8*)(lds + PG8_SA(b, h) + aoff + m * 2048 + 1024); dst[m].set(f0_, f1_); } } while (0)
; #define PG8_LDB(dst, b, h) do { _Pragma("unroll") for (int n = 0; n < 2; ++n) { const bf16x8 f0_ = *(const PG8_LAS bf16x8*)(lds + PG8_SB(b, h) + boff + n * 2048), f1_ = *(const PG8_LAS bf16x8*)(lds + PG8_SB(b, h) + boff + n * 2048 + 1024); dst[n].set(f0_, f1_); } } while (0)
; #define PG8_WAIT_V(n) asm volatile("s_waitcnt vmcnt(" #n ")" ::: "memory")
; #define PG8_WAIT_L(n) asm volatile("s_waitcnt lgkmcnt(" #n ")" ::: "memory")
; #define PG8_BAR __builtin_amdgcn_s_barrier()
; #define PG8_SCHED __builtin_amdgcn_sched_barrier(0)
; template <class Epi, class Sched, bool ALIGN_EPI = false, bool SP2 = false>
; __device__ __forceinline__ void gemm_phase(PG8_LAS unsigned char* lds, const Gemm g, const Sched& S, const Epi& E) {
;     ...
;             PG8_WAIT_V(8); PG8_WAIT_L(0); PG8_BAR; PG8_MMA(1, 0, At, B0); PG8_MMA(1, 1, At, B1); PG8_BAR; PG8_SCHED;
;             PG8_LDB(B0, 1, 0); PG8_LDB(B1, 1, 1); PG8_SCHED; PG8_LDA(At, 1, 0); PG8_STAGE(PG8_SA(0, 1), a2 + hstep, voffA);
;             PG8_WAIT_V(8); PG8_WAIT_L(0); PG8_BAR; PG8_MMA(0, 0, At, B0); PG8_MMA(0, 1, At, B1); PG8_BAR; PG8_SCHED;
	s_setprio 1
	s_waitcnt lgkmcnt(0)
	v_mfma_f32_16x16x32_bf16 v[62:65], v[156:159], v[188:191], v[62:65]
	v_mfma_f32_16x16x32_bf16 v[58:61], v[164:167], v[188:191], v[58:61]
	v_mfma_f32_16x16x32_bf16 v[46:49], v[156:159], v[196:199], v[46:49]
	v_mfma_f32_16x16x32_bf16 v[42:45], v[164:167], v[196:199], v[42:45]
	v_mfma_f32_16x16x32_bf16 v[30:33], v[156:159], v[204:207], v[30:33]
	v_mfma_f32_16x16x32_bf16 v[26:29], v[164:167], v[204:207], v[26:29]
	v_mfma_f32_16x16x32_bf16 v[14:17], v[156:159], v[216:219], v[14:17]
	v_mfma_f32_16x16x32_bf16 v[6:9], v[164:167], v[216:219], v[6:9]
	v_mfma_f32_16x16x32_bf16 v[62:65], v[160:163], v[192:195], v[62:65]
	v_mfma_f32_16x16x32_bf16 v[58:61], v[168:171], v[192:195], v[58:61]
	v_mfma_f32_16x16x32_bf16 v[46:49], v[160:163], v[200:203], v[46:49]
	v_mfma_f32_16x16x32_bf16 v[42:45], v[168:171], v[200:203], v[42:45]
	v_mfma_f32_16x16x32_bf16 v[30:33], v[160:163], v[212:215], v[30:33]
	v_mfma_f32_16x16x32_bf16 v[26:29], v[168:171], v[212:215], v[26:29]
	v_mfma_f32_16x16x32_bf16 v[14:17], v[160:163], v[220:223], v[14:17]
	v_mfma_f32_16x16x32_bf16 v[6:9], v[168:171], v[220:223], v[6:9]
	s_setprio 0
	s_setprio 1
	v_mfma_f32_16x16x32_bf16 v[54:57], v[172:175], v[188:191], v[54:57]
	v_mfma_f32_16x16x32_bf16 v[50:53], v[180:183], v[188:191], v[50:53]
	v_mfma_f32_16x16x32_bf16 v[38:41], v[172:175], v[196:199], v[38:41]
	v_mfma_f32_16x16x32_bf16 v[34:37], v[180:183], v[196:199], v[34:37]
	v_mfma_f32_16x16x32_bf16 v[22:25], v[172:175], v[204:207], v[22:25]
	v_mfma_f32_16x16x32_bf16 v[18:21], v[180:183], v[204:207], v[18:21]
	v_mfma_f32_16x16x32_bf16 v[10:13], v[172:175], v[216:219], v[10:13]
	v_mfma_f32_16x16x32_bf16 v[2:5], v[180:183], v[216:219], v[2:5]
	v_mfma_f32_16x16x32_bf16 v[54:57], v[176:179], v[192:195], v[54:57]
	v_mfma_f32_16x16x32_bf16 v[50:53], v[184:187], v[192:195], v[50:53]
	v_mfma_f32_16x16x32_bf16 v[38:41], v[176:179], v[200:203], v[38:41]
	v_mfma_f32_16x16x32_bf16 v[34:37], v[184:187], v[200:203], v[34:37]
	v_mfma_f32_16x16x32_bf16 v[22:25], v[176:179], v[212:215], v[22:25]
	v_mfma_f32_16x16x32_bf16 v[18:21], v[184:187], v[212:215], v[18:21]
	v_mfma_f32_16x16x32_bf16 v[10:13], v[176:179], v[220:223], v[10:13]
	v_mfma_f32_16x16x32_bf16 v[2:5], v[184:187], v[220:223], v[2:5]
	s_setprio 0
	s_barrier
	ds_read_b128 v[188:191], v154 offset:32768
	ds_read_b128 v[192:195], v154 offset:33792
	ds_read_b128 v[196:199], v154 offset:34816
	ds_read_b128 v[200:203], v154 offset:35840
	ds_read_b128 v[204:207], v154 offset:36864
	ds_read_b128 v[212:215], v154 offset:37888
	ds_read_b128 v[216:219], v154 offset:38912
	ds_read_b128 v[220:223], v154 offset:39936
	s_add_i32 s33, 0, 0x18000
	s_add_i32 s63, 0, 0x1c000
	v_add_u32_e32 v168, s33, v1
	v_add_u32_e32 v184, s63, v1
	ds_read_b128 v[156:159], v168
	ds_read_b128 v[160:163], v168 offset:1024
	ds_read_b128 v[164:167], v168 offset:2048
	ds_read_b128 v[168:171], v168 offset:3072
	ds_read_b128 v[172:175], v184
	ds_read_b128 v[176:179], v184 offset:1024
	ds_read_b128 v[180:183], v184 offset:2048
	ds_read_b128 v[184:187], v184 offset:3072
	s_add_u32 s0, s34, s12
	s_addc_u32 s1, s35, s13
	s_mov_b32 m0, s42
	v_lshl_add_u64 v[232:233], s[0:1], 0, v[130:131]
	s_mov_b32 m0, s40
	s_nop 0
	global_load_lds_dwordx4 v[228:229], off
	s_mov_b32 m0, s41
	s_nop 0
	global_load_lds_dwordx4 v[230:231], off
	s_mov_b32 m0, s42
	s_nop 0
	global_load_lds_dwordx4 v[232:233], off
	v_lshl_add_u64 v[232:233], s[0:1], 0, v[134:135]
	s_mov_b32 m0, s43
	s_nop 0
	global_load_lds_dwordx4 v[232:233], off
	s_waitcnt vmcnt(8)
	s_waitcnt lgkmcnt(0)
	s_barrier
; #define PG8_STAGE(bufoff, gbase, voff) do { _Pragma("unroll") for (int _i = 0; _i < 2; ++_i) \
;         __builtin_amdgcn_global_load_lds((const unsigned*)((const char*)(gbase) + (voff)[_i]), (PG8_LAS unsigned*)(lds + (bufoff) + ldsw + _i * 8192), 16, 0, 0); } while (0)
; #define PG8_LDA(dst, b, h) do { _Pragma("unroll") for (int m = 0; m < 4; ++m) { const bf16x8 f0_ = *(const PG8_LAS bf16x8*)(lds + PG8_SA(b, h) + aoff + m * 2048), f1_ = *(const PG8_LAS bf16x8*)(lds + PG8_SA(b, h) + aoff + m * 2048 + 1024); dst[m].set(f0_, f1_); } } while (0)
; #define PG8_WAIT_V(n) asm volatile("s_waitcnt vmcnt(" #n ")" ::: "memory")
; #define PG8_WAIT_L(n) asm volatile("s_waitcnt lgkmcnt(" #n ")" ::: "memory")
; #define PG8_BAR __builtin_amdgcn_s_barrier()
; #define PG8_SCHED __builtin_amdgcn_sched_barrier(0)
; template <class Epi, class Sched, bool ALIGN_EPI = false, bool SP2 = false>
; __device__ __forceinline__ void gemm_phase(PG8_LAS unsigned char* lds, const Gemm g, const Sched& S, const Epi& E) {
;     ...
;             PG8_WAIT_V(8); PG8_WAIT_L(0); PG8_BAR; PG8_MMA(0, 0, At, B0); PG8_MMA(0, 1, At, B1); PG8_BAR; PG8_SCHED;
;             PG8_LDA(At, 1, 1); PG8_STAGE(PG8_SB(1, 0), b3, voffB); PG8_STAGE(PG8_SB(1, 1), b3 + hstepB, voffB); PG8_STAGE(PG8_SA(1, 0), a3, voffA);
	s_setprio 1
	s_waitcnt lgkmcnt(0)
	v_mfma_f32_16x16x32_bf16 v[126:129], v[156:159], v[188:191], v[126:129]
	v_mfma_f32_16x16x32_bf16 v[122:125], v[164:167], v[188:191], v[122:125]
	v_mfma_f32_16x16x32_bf16 v[110:113], v[156:159], v[196:199], v[110:113]
	v_mfma_f32_16x16x32_bf16 v[106:109], v[164:167], v[196:199], v[106:109]
	v_mfma_f32_16x16x32_bf16 v[94:97], v[156:159], v[204:207], v[94:97]
	v_mfma_f32_16x16x32_bf16 v[90:93], v[164:167], v[204:207], v[90:93]
	v_mfma_f32_16x16x32_bf16 v[78:81], v[156:159], v[216:219], v[78:81]
	v_mfma_f32_16x16x32_bf16 v[74:77], v[164:167], v[216:219], v[74:77]
	v_mfma_f32_16x16x32_bf16 v[126:129], v[160:163], v[192:195], v[126:129]
	v_mfma_f32_16x16x32_bf16 v[122:125], v[168:171], v[192:195], v[122:125]
	v_mfma_f32_16x16x32_bf16 v[110:113], v[160:163], v[200:203], v[110:113]
	v_mfma_f32_16x16x32_bf16 v[106:109], v[168:171], v[200:203], v[106:109]
	v_mfma_f32_16x16x32_bf16 v[94:97], v[160:163], v[212:215], v[94:97]
	v_mfma_f32_16x16x32_bf16 v[90:93], v[168:171], v[212:215], v[90:93]
	v_mfma_f32_16x16x32_bf16 v[78:81], v[160:163], v[220:223], v[78:81]
	v_mfma_f32_16x16x32_bf16 v[74:77], v[168:171], v[220:223], v[74:77]
	s_setprio 0
	s_setprio 1
	v_mfma_f32_16x16x32_bf16 v[118:121], v[172:175], v[188:191], v[118:121]
	v_mfma_f32_16x16x32_bf16 v[114:117], v[180:183], v[188:191], v[114:117]
	v_mfma_f32_16x16x32_bf16 v[102:105], v[172:175], v[196:199], v[102:105]
	v_mfma_f32_16x16x32_bf16 v[98:101], v[180:183], v[196:199], v[98:101]
	v_mfma_f32_16x16x32_bf16 v[86:89], v[172:175], v[204:207], v[86:89]
	v_mfma_f32_16x16x32_bf16 v[82:85], v[180:183], v[204:207], v[82:85]
	v_mfma_f32_16x16x32_bf16 v[70:73], v[172:175], v[216:219], v[70:73]
	v_mfma_f32_16x16x32_bf16 v[66:69], v[180:183], v[216:219], v[66:69]
	v_mfma_f32_16x16x32_bf16 v[118:121], v[176:179], v[192:195], v[118:121]
	v_mfma_f32_16x16x32_bf16 v[114:117], v[184:187], v[192:195], v[114:117]
	v_mfma_f32_16x16x32_bf16 v[102:105], v[176:179], v[200:203], v[102:105]
	v_mfma_f32_16x16x32_bf16 v[98:101], v[184:187], v[200:203], v[98:101]
	v_mfma_f32_16x16x32_bf16 v[86:89], v[176:179], v[212:215], v[86:89]
	v_mfma_f32_16x16x32_bf16 v[82:85], v[184:187], v[212:215], v[82:85]
	v_mfma_f32_16x16x32_bf16 v[70:73], v[176:179], v[220:223], v[70:73]
	v_mfma_f32_16x16x32_bf16 v[66:69], v[184:187], v[220:223], v[66:69]
	s_setprio 0
	s_barrier
	ds_read_b128 v[188:191], v154 offset:49152
	ds_read_b128 v[192:195], v154 offset:50176
	ds_read_b128 v[196:199], v154 offset:51200
	ds_read_b128 v[200:203], v154 offset:52224
	ds_read_b128 v[204:207], v154 offset:53248
	ds_read_b128 v[212:215], v154 offset:54272
	ds_read_b128 v[216:219], v154 offset:55296
	ds_read_b128 v[220:223], v154 offset:56320
	s_add_i32 s0, s33, s39
	v_lshl_add_u64 v[148:149], v[148:149], 0, s[22:23]
	s_mov_b32 m0, s0
	s_nop 0
	global_load_lds_dwordx4 v[148:149], off
	v_lshl_add_u64 v[148:149], v[208:209], 0, s[22:23]
	s_add_i32 m0, s0, 0x2000
	s_add_i32 s0, s63, s39
	global_load_lds_dwordx4 v[148:149], off
	v_lshl_add_u64 v[148:149], v[224:225], 0, s[22:23]
	s_mov_b32 m0, s0
	s_nop 0
	global_load_lds_dwordx4 v[148:149], off
	v_lshl_add_u64 v[148:149], v[226:227], 0, s[22:23]
	s_add_i32 m0, s0, 0x2000
	s_nop 0
	global_load_lds_dwordx4 v[148:149], off
	s_cmp_ge_i32 s61, s47
	s_cbranch_scc0 .Lkr3_b
	v_lshl_add_u64 v[148:149], v[228:229], 0, s[22:23]
	s_mov_b32 m0, s45
	s_nop 0
	global_load_lds_dwordx4 v[148:149], off
	v_lshl_add_u64 v[148:149], v[230:231], 0, s[22:23]
	s_mov_b32 m0, s46
	s_nop 0
	global_load_lds_dwordx4 v[148:149], off

; #define PG8_STAGE(bufoff, gbase, voff) do { _Pragma("unroll") for (int _i = 0; _i < 2; ++_i) \
;         __builtin_amdgcn_global_load_lds((const unsigned*)((const char*)(gbase) + (voff)[_i]), (PG8_LAS unsigned*)(lds + (bufoff) + ldsw + _i * 8192), 16, 0, 0); } while (0)
; #define PG8_LDA(dst, b, h) do { _Pragma("unroll") for (int m = 0; m < 4; ++m) { const bf16x8 f0_ = *(const PG8_LAS bf16x8*)(lds + PG8_SA(b, h) + aoff + m * 2048), f1_ = *(const PG8_LAS bf16x8*)(lds + PG8_SA(b, h) + aoff + m * 2048 + 1024); dst[m].set(f0_, f1_); } } while (0)
; #define PG8_LDB(dst, b, h) do { _Pragma("unroll") for (int n = 0; n < 2; ++n) { const bf16x8 f0_ = *(const PG8_LAS bf16x8*)(lds + PG8_SB(b, h) + boff + n * 2048), f1_ = *(const PG8_LAS bf16x8*)(lds + PG8_SB(b, h) + boff + n * 2048 + 1024); dst[n].set(f0_, f1_); } } while (0)
; #define PG8_WAIT_V(n) asm volatile("s_waitcnt vmcnt(" #n ")" ::: "memory")
; #define PG8_WAIT_L(n) asm volatile("s_waitcnt lgkmcnt(" #n ")" ::: "memory")
; #define PG8_BAR __builtin_amdgcn_s_barrier()
; #define PG8_SCHED __builtin_amdgcn_sched_barrier(0)
; template <class Epi, class Sched, bool ALIGN_EPI = false, bool SP2 = false>
; __device__ __forceinline__ void gemm_phase(PG8_LAS unsigned char* lds, const Gemm g, const Sched& S, const Epi& E) {
;     ...
;             const bool last = (t == nt - 2);
;             const char* a1 = cA + (size_t)(t + 1) * kstep;
;             const char* a2 = last ? nA : cA + (size_t)(t + 2) * kstep; const char* b2 = last ? nB : cB + (size_t)(t + 2) * kstep;
;             const char* a3 = a2 + kstep; const char* b3 = b2 + kstep;
;             if (last && has_next) S.a_ready(nxt);
;             if constexpr (SP2) {
;             PG8_LDB(B0, 0, 0); PG8_LDB(B1, 0, 1); PG8_SCHED; PG8_LDA(At, 0, 0); PG8_STAGE(PG8_SA(1, 1), a1 + hstep, voffA);
;             PG8_WAIT_V(8); PG8_WAIT_L(0); PG8_BAR; PG8_MMA(0, 0, At, B0); PG8_MMA(0, 1, At, B1); PG8_BAR; PG8_SCHED;
;             PG8_LDA(At, 0, 1); PG8_STAGE(PG8_SB(0, 0), b2, voffB); PG8_STAGE(PG8_SB(0, 1), b2 + hstepB, voffB); PG8_STAGE(PG8_SA(0, 0), a2, voffA);
;             PG8_WAIT_V(8); PG8_WAIT_L(0); PG8_BAR; PG8_MMA(1, 0, At, B0); PG8_MMA(1, 1, At, B1); PG8_BAR; PG8_SCHED;
.LBB0_1592:
	ds_read_b128 v[156:159], v152
	ds_read_b128 v[160:163], v152 offset:1024
	ds_read_b128 v[164:167], v152 offset:2048
	ds_read_b128 v[168:171], v152 offset:3072
	ds_read_b128 v[172:175], v153
	ds_read_b128 v[176:179], v153 offset:1024
	ds_read_b128 v[180:183], v153 offset:2048
	ds_read_b128 v[184:187], v153 offset:3072
	ds_read_b128 v[188:191], v154
	ds_read_b128 v[192:195], v154 offset:1024
	ds_read_b128 v[196:199], v154 offset:2048
	ds_read_b128 v[200:203], v154 offset:3072
	ds_read_b128 v[204:207], v154 offset:4096
	ds_read_b128 v[212:215], v154 offset:5120
	ds_read_b128 v[216:219], v154 offset:6144
	ds_read_b128 v[220:223], v154 offset:7168
	s_add_i32 s61, s34, 2
	s_add_u32 s0, s30, 0x80
	s_addc_u32 s1, s31, 0
	s_cmp_eq_u32 s49, s34
	s_cselect_b32 s34, s6, s0
	s_cselect_b32 s35, s7, s1
	s_cselect_b32 s1, s29, s59
	s_cselect_b32 s0, s28, s58
	s_cmp_eq_u32 s99, 0
	s_cbranch_scc1 .Lkr4_a
	v_lshl_add_u64 v[228:229], v[228:229], 0, s[22:23]
	s_mov_b32 m0, s46
	v_lshl_add_u64 v[230:231], v[230:231], 0, s[22:23]
	global_load_lds_dwordx4 v[228:229], off
	s_mov_b32 m0, s47
	s_nop 0
	global_load_lds_dwordx4 v[230:231], off
.Lkr4_a:
	v_lshl_add_u64 v[148:149], s[30:31], 0, v[140:141]
	s_add_i32 m0, s40, 0xc000
	s_nop 0
	global_load_lds_dwordx4 v[148:149], off
	v_lshl_add_u64 v[148:149], s[30:31], 0, v[142:143]
	s_add_i32 m0, s40, 0xe000
	s_nop 0
	global_load_lds_dwordx4 v[148:149], off
	s_waitcnt vmcnt(8)
	s_waitcnt lgkmcnt(0)
	s_barrier
	s_setprio 1
	s_waitcnt lgkmcnt(0)
	v_mfma_f32_16x16x32_bf16 v[126:129], v[156:159], v[188:191], v[126:129]
	v_mfma_f32_16x16x32_bf16 v[122:125], v[164:167], v[188:191], v[122:125]
	v_mfma_f32_16x16x32_bf16 v[110:113], v[156:159], v[196:199], v[110:113]
	v_mfma_f32_16x16x32_bf16 v[106:109], v[164:167], v[196:199], v[106:109]
	v_mfma_f32_16x16x32_bf16 v[94:97], v[156:159], v[204:207], v[94:97]
	v_mfma_f32_16x16x32_bf16 v[90:93], v[164:167], v[204:207], v[90:93]
	v_mfma_f32_16x16x32_bf16 v[78:81], v[156:159], v[216:219], v[78:81]
	v_mfma_f32_16x16x32_bf16 v[74:77], v[164:167], v[216:219], v[74:77]
	v_mfma_f32_16x16x32_bf16 v[126:129], v[160:163], v[192:195], v[126:129]
	v_mfma_f32_16x16x32_bf16 v[122:125], v[168:171], v[192:195], v[122:125]
	v_mfma_f32_16x16x32_bf16 v[110:113], v[160:163], v[200:203], v[110:113]
	v_mfma_f32_16x16x32_bf16 v[106:109], v[168:171], v[200:203], v[106:109]
	v_mfma_f32_16x16x32_bf16 v[94:97], v[160:163], v[212:215], v[94:97]
	v_mfma_f32_16x16x32_bf16 v[90:93], v[168:171], v[212:215], v[90:93]
	v_mfma_f32_16x16x32_bf16 v[78:81], v[160:163], v[220:223], v[78:81]
	v_mfma_f32_16x16x32_bf16 v[74:77], v[168:171], v[220:223], v[74:77]
	s_setprio 0
	s_setprio 1
	v_mfma_f32_16x16x32_bf16 v[118:121], v[172:175], v[188:191], v[118:121]
	v_mfma_f32_16x16x32_bf16 v[114:117], v[180:183], v[188:191], v[114:117]
	v_mfma_f32_16x16x32_bf16 v[102:105], v[172:175], v[196:199], v[102:105]
	v_mfma_f32_16x16x32_bf16 v[98:101], v[180:183], v[196:199], v[98:101]
	v_mfma_f32_16x16x32_bf16 v[86:89], v[172:175], v[204:207], v[86:89]
	v_mfma_f32_16x16x32_bf16 v[82:85], v[180:183], v[204:207], v[82:85]
	v_mfma_f32_16x16x32_bf16 v[70:73], v[172:175], v[216:219], v[70:73]
	v_mfma_f32_16x16x32_bf16 v[66:69], v[180:183], v[216:219], v[66:69]
	v_mfma_f32_16x16x32_bf16 v[118:121], v[176:179], v[192:195], v[118:121]
	v_mfma_f32_16x16x32_bf16 v[114:117], v[184:187], v[192:195], v[114:117]
	v_mfma_f32_16x16x32_bf16 v[102:105], v[176:179], v[200:203], v[102:105]
	v_mfma_f32_16x16x32_bf16 v[98:101], v[184:187], v[200:203], v[98:101]
	v_mfma_f32_16x16x32_bf16 v[86:89], v[176:179], v[212:215], v[86:89]
	v_mfma_f32_16x16x32_bf16 v[82:85], v[184:187], v[212:215], v[82:85]
	v_mfma_f32_16x16x32_bf16 v[70:73], v[176:179], v[220:223], v[70:73]
	v_mfma_f32_16x16x32_bf16 v[66:69], v[184:187], v[220:223], v[66:69]
	s_setprio 0
	s_barrier
	ds_read_b128 v[188:191], v154 offset:16384
	ds_read_b128 v[192:195], v154 offset:17408
	ds_read_b128 v[196:199], v154 offset:18432
	ds_read_b128 v[200:203], v154 offset:19456
	ds_read_b128 v[204:207], v154 offset:20480
	ds_read_b128 v[212:215], v154 offset:21504
	ds_read_b128 v[216:219], v154 offset:22528
	ds_read_b128 v[220:223], v154 offset:23552
	s_add_i32 s33, s52, s39
	v_lshl_add_u64 v[148:149], s[0:1], 0, v[132:133]
	s_mov_b32 m0, s33
	s_nop 0
	global_load_lds_dwordx4 v[148:149], off
	s_add_i32 m0, s33, 0x2000
	v_lshl_add_u64 v[208:209], s[0:1], 0, v[136:137]
	s_add_u32 s0, s0, s14
	s_addc_u32 s1, s1, s15
	s_add_i32 s33, s53, s39
	global_load_lds_dwordx4 v[208:209], off
	v_lshl_add_u64 v[224:225], s[0:1], 0, v[132:133]
	s_mov_b32 m0, s33
	v_lshl_add_u64 v[226:227], s[0:1], 0, v[136:137]
	global_load_lds_dwordx4 v[224:225], off
	s_add_i32 m0, s33, 0x2000
	v_lshl_add_u64 v[228:229], s[34:35], 0, v[130:131]
	global_load_lds_dwordx4 v[226:227], off
	v_lshl_add_u64 v[230:231], s[34:35], 0, v[134:135]
	s_waitcnt vmcnt(6)
	s_waitcnt lgkmcnt(0)
	s_barrier
; #define PG8_STAGE(bufoff, gbase, voff) do { _Pragma("unroll") for (int _i = 0; _i < 2; ++_i) \
;         __builtin_amdgcn_global_load_lds((const unsigned*)((const char*)(gbase) + (voff)[_i]), (PG8_LAS unsigned*)(lds + (bufoff) + ldsw + _i * 8192), 16, 0, 0); } while (0)
; #define PG8_LDA(dst, b, h) do { _Pragma("unroll") for (int m = 0; m < 4; ++m) { const bf16x8 f0_ = *(const PG8_LAS bf16x8*)(lds + PG8_SA(b, h) + aoff + m * 2048), f1_ = *(const PG8_LAS bf16x8*)(lds + PG8_SA(b, h) + aoff + m * 2048 + 1024); dst[m].set(f0_, f1_); } } while (0)
; #define PG8_LDB(dst, b, h) do { _Pragma("unroll") for (int n = 0; n < 2; ++n) { const bf16x8 f0_ = *(const PG8_LAS bf16x8*)(lds + PG8_SB(b, h) + boff + n * 2048), f1_ = *(const PG8_LAS bf16x8*)(lds + PG8_SB(b, h) + boff + n * 2048 + 1024); dst[n].set(f0_, f1_); } } while (0)
; #define PG8_WAIT_V(n) asm volatile("s_waitcnt vmcnt(" #n ")" ::: "memory")
; #define PG8_WAIT_L(n) asm volatile("s_waitcnt lgkmcnt(" #n ")" ::: "memory")
; #define PG8_BAR __builtin_amdgcn_s_barrier()
; #define PG8_SCHED __builtin_amdgcn_sched_barrier(0)
; template <class Epi, class Sched, bool ALIGN_EPI = false, bool SP2 = false>
; __device__ __forceinline__ void gemm_phase(PG8_LAS unsigned char* lds, const Gemm g, const Sched& S, const Epi& E) {
;     ...
;             PG8_WAIT_V(8); PG8_WAIT_L(0); PG8_BAR; PG8_MMA(1, 0, At, B0); PG8_MMA(1, 1, At, B1); PG8_BAR; PG8_SCHED;
;             PG8_LDB(B0, 1, 0); PG8_LDB(B1, 1, 1); PG8_SCHED; PG8_LDA(At, 1, 0); PG8_STAGE(PG8_SA(0, 1), a2 + hstep, voffA);
;             PG8_WAIT_V(8); PG8_WAIT_L(0); PG8_BAR; PG8_MMA(0, 0, At, B0); PG8_MMA(0, 1, At, B1); PG8_BAR; PG8_SCHED;
	s_setprio 1
	s_waitcnt lgkmcnt(0)
	v_mfma_f32_16x16x32_bf16 v[62:65], v[156:159], v[188:191], v[62:65]
	v_mfma_f32_16x16x32_bf16 v[58:61], v[164:167], v[188:191], v[58:61]
	v_mfma_f32_16x16x32_bf16 v[46:49], v[156:159], v[196:199], v[46:49]
	v_mfma_f32_16x16x32_bf16 v[42:45], v[164:167], v[196:199], v[42:45]
	v_mfma_f32_16x16x32_bf16 v[30:33], v[156:159], v[204:207], v[30:33]
	v_mfma_f32_16x16x32_bf16 v[26:29], v[164:167], v[204:207], v[26:29]
	v_mfma_f32_16x16x32_bf16 v[14:17], v[156:159], v[216:219], v[14:17]
	v_mfma_f32_16x16x32_bf16 v[6:9], v[164:167], v[216:219], v[6:9]
	v_mfma_f32_16x16x32_bf16 v[62:65], v[160:163], v[192:195], v[62:65]
	v_mfma_f32_16x16x32_bf16 v[58:61], v[168:171], v[192:195], v[58:61]
	v_mfma_f32_16x16x32_bf16 v[46:49], v[160:163], v[200:203], v[46:49]
	v_mfma_f32_16x16x32_bf16 v[42:45], v[168:171], v[200:203], v[42:45]
	v_mfma_f32_16x16x32_bf16 v[30:33], v[160:163], v[212:215], v[30:33]
	v_mfma_f32_16x16x32_bf16 v[26:29], v[168:171], v[212:215], v[26:29]
	v_mfma_f32_16x16x32_bf16 v[14:17], v[160:163], v[220:223], v[14:17]
	v_mfma_f32_16x16x32_bf16 v[6:9], v[168:171], v[220:223], v[6:9]
	s_setprio 0
	s_setprio 1
	v_mfma_f32_16x16x32_bf16 v[54:57], v[172:175], v[188:191], v[54:57]
	v_mfma_f32_16x16x32_bf16 v[50:53], v[180:183], v[188:191], v[50:53]
	v_mfma_f32_16x16x32_bf16 v[38:41], v[172:175], v[196:199], v[38:41]
	v_mfma_f32_16x16x32_bf16 v[34:37], v[180:183], v[196:199], v[34:37]
	v_mfma_f32_16x16x32_bf16 v[22:25], v[172:175], v[204:207], v[22:25]
	v_mfma_f32_16x16x32_bf16 v[18:21], v[180:183], v[204:207], v[18:21]
	v_mfma_f32_16x16x32_bf16 v[10:13], v[172:175], v[216:219], v[10:13]
	v_mfma_f32_16x16x32_bf16 v[2:5], v[180:183], v[216:219], v[2:5]
	v_mfma_f32_16x16x32_bf16 v[54:57], v[176:179], v[192:195], v[54:57]
	v_mfma_f32_16x16x32_bf16 v[50:53], v[184:187], v[192:195], v[50:53]
	v_mfma_f32_16x16x32_bf16 v[38:41], v[176:179], v[200:203], v[38:41]
	v_mfma_f32_16x16x32_bf16 v[34:37], v[184:187], v[200:203], v[34:37]
	v_mfma_f32_16x16x32_bf16 v[22:25], v[176:179], v[212:215], v[22:25]
	v_mfma_f32_16x16x32_bf16 v[18:21], v[184:187], v[212:215], v[18:21]
	v_mfma_f32_16x16x32_bf16 v[10:13], v[176:179], v[220:223], v[10:13]
	v_mfma_f32_16x16x32_bf16 v[2:5], v[184:187], v[220:223], v[2:5]
	s_setprio 0
	s_barrier
	ds_read_b128 v[188:191], v154 offset:32768
	ds_read_b128 v[192:195], v154 offset:33792
	ds_read_b128 v[196:199], v154 offset:34816
	ds_read_b128 v[200:203], v154 offset:35840
	ds_read_b128 v[204:207], v154 offset:36864
	ds_read_b128 v[212:215], v154 offset:37888
	ds_read_b128 v[216:219], v154 offset:38912
	ds_read_b128 v[220:223], v154 offset:39936
	s_add_i32 s33, 0, 0x18000
	s_add_i32 s63, 0, 0x1c000
	v_add_u32_e32 v168, s33, v1
	v_add_u32_e32 v184, s63, v1
	ds_read_b128 v[156:159], v168
	ds_read_b128 v[160:163], v168 offset:1024
	ds_read_b128 v[164:167], v168 offset:2048
	ds_read_b128 v[168:171], v168 offset:3072
	ds_read_b128 v[172:175], v184
	ds_read_b128 v[176:179], v184 offset:1024
	ds_read_b128 v[180:183], v184 offset:2048
	ds_read_b128 v[184:187], v184 offset:3072
	s_add_u32 s0, s34, s12
	s_addc_u32 s1, s35, s13
	s_mov_b32 m0, s42
	v_lshl_add_u64 v[232:233], s[0:1], 0, v[130:131]
	s_mov_b32 m0, s40
	s_nop 0
	global_load_lds_dwordx4 v[228:229], off
	s_mov_b32 m0, s41
	s_nop 0
	global_load_lds_dwordx4 v[230:231], off
	s_mov_b32 m0, s42
	s_nop 0
	global_load_lds_dwordx4 v[232:233], off
	v_lshl_add_u64 v[232:233], s[0:1], 0, v[134:135]
	s_mov_b32 m0, s43
	s_nop 0
	global_load_lds_dwordx4 v[232:233], off
	s_waitcnt vmcnt(8)
	s_waitcnt lgkmcnt(0)
	s_barrier
; #define PG8_STAGE(bufoff, gbase, voff) do { _Pragma("unroll") for (int _i = 0; _i < 2; ++_i) \
;         __builtin_amdgcn_global_load_lds((const unsigned*)((const char*)(gbase) + (voff)[_i]), (PG8_LAS unsigned*)(lds + (bufoff) + ldsw + _i * 8192), 16, 0, 0); } while (0)
; #define PG8_LDA(dst, b, h) do { _Pragma("unroll") for (int m = 0; m < 4; ++m) { const bf16x8 f0_ = *(const PG8_LAS bf16x8*)(lds + PG8_SA(b, h) + aoff + m * 2048), f1_ = *(const PG8_LAS bf16x8*)(lds + PG8_SA(b, h) + aoff + m * 2048 + 1024); dst[m].set(f0_, f1_); } } while (0)
; #define PG8_WAIT_V(n) asm volatile("s_waitcnt vmcnt(" #n ")" ::: "memory")
; #define PG8_WAIT_L(n) asm volatile("s_waitcnt lgkmcnt(" #n ")" ::: "memory")
; #define PG8_BAR __builtin_amdgcn_s_barrier()
; #define PG8_SCHED __builtin_amdgcn_sched_barrier(0)
; template <class Epi, class Sched, bool ALIGN_EPI = false, bool SP2 = false>
; __device__ __forceinline__ void gemm_phase(PG8_LAS unsigned char* lds, const Gemm g, const Sched& S, const Epi& E) {
;     ...
;             PG8_WAIT_V(8); PG8_WAIT_L(0); PG8_BAR; PG8_MMA(0, 0, At, B0); PG8_MMA(0, 1, At, B1); PG8_BAR; PG8_SCHED;
;             PG8_LDA(At, 1, 1); PG8_STAGE(PG8_SB(1, 0), b3, voffB); PG8_STAGE(PG8_SB(1, 1), b3 + hstepB, voffB); PG8_STAGE(PG8_SA(1, 0), a3, voffA);
	s_setprio 1
	s_waitcnt lgkmcnt(0)
	v_mfma_f32_16x16x32_bf16 v[126:129], v[156:159], v[188:191], v[126:129]
	v_mfma_f32_16x16x32_bf16 v[122:125], v[164:167], v[188:191], v[122:125]
	v_mfma_f32_16x16x32_bf16 v[110:113], v[156:159], v[196:199], v[110:113]
	v_mfma_f32_16x16x32_bf16 v[106:109], v[164:167], v[196:199], v[106:109]
	v_mfma_f32_16x16x32_bf16 v[94:97], v[156:159], v[204:207], v[94:97]
	v_mfma_f32_16x16x32_bf16 v[90:93], v[164:167], v[204:207], v[90:93]
	v_mfma_f32_16x16x32_bf16 v[78:81], v[156:159], v[216:219], v[78:81]
	v_mfma_f32_16x16x32_bf16 v[74:77], v[164:167], v[216:219], v[74:77]
	v_mfma_f32_16x16x32_bf16 v[126:129], v[160:163], v[192:195], v[126:129]
	v_mfma_f32_16x16x32_bf16 v[122:125], v[168:171], v[192:195], v[122:125]
	v_mfma_f32_16x16x32_bf16 v[110:113], v[160:163], v[200:203], v[110:113]
	v_mfma_f32_16x16x32_bf16 v[106:109], v[168:171], v[200:203], v[106:109]
	v_mfma_f32_16x16x32_bf16 v[94:97], v[160:163], v[212:215], v[94:97]
	v_mfma_f32_16x16x32_bf16 v[90:93], v[168:171], v[212:215], v[90:93]
	v_mfma_f32_16x16x32_bf16 v[78:81], v[160:163], v[220:223], v[78:81]
	v_mfma_f32_16x16x32_bf16 v[74:77], v[168:171], v[220:223], v[74:77]
	s_setprio 0
	s_setprio 1
	v_mfma_f32_16x16x32_bf16 v[118:121], v[172:175], v[188:191], v[118:121]
	v_mfma_f32_16x16x32_bf16 v[114:117], v[180:183], v[188:191], v[114:117]
	v_mfma_f32_16x16x32_bf16 v[102:105], v[172:175], v[196:199], v[102:105]
	v_mfma_f32_16x16x32_bf16 v[98:101], v[180:183], v[196:199], v[98:101]
	v_mfma_f32_16x16x32_bf16 v[86:89], v[172:175], v[204:207], v[86:89]
	v_mfma_f32_16x16x32_bf16 v[82:85], v[180:183], v[204:207], v[82:85]
	v_mfma_f32_16x16x32_bf16 v[70:73], v[172:175], v[216:219], v[70:73]
	v_mfma_f32_16x16x32_bf16 v[66:69], v[180:183], v[216:219], v[66:69]
	v_mfma_f32_16x16x32_bf16 v[118:121], v[176:179], v[192:195], v[118:121]
	v_mfma_f32_16x16x32_bf16 v[114:117], v[184:187], v[192:195], v[114:117]
	v_mfma_f32_16x16x32_bf16 v[102:105], v[176:179], v[200:203], v[102:105]
	v_mfma_f32_16x16x32_bf16 v[98:101], v[184:187], v[200:203], v[98:101]
	v_mfma_f32_16x16x32_bf16 v[86:89], v[176:179], v[212:215], v[86:89]
	v_mfma_f32_16x16x32_bf16 v[82:85], v[184:187], v[212:215], v[82:85]
	v_mfma_f32_16x16x32_bf16 v[70:73], v[176:179], v[220:223], v[70:73]
	v_mfma_f32_16x16x32_bf16 v[66:69], v[184:187], v[220:223], v[66:69]
	s_setprio 0
	s_barrier
	ds_read_b128 v[188:191], v154 offset:49152
	ds_read_b128 v[192:195], v154 offset:50176
	ds_read_b128 v[196:199], v154 offset:51200
	ds_read_b128 v[200:203], v154 offset:52224
	ds_read_b128 v[204:207], v154 offset:53248
	ds_read_b128 v[212:215], v154 offset:54272
	ds_read_b128 v[216:219], v154 offset:55296
	ds_read_b128 v[220:223], v154 offset:56320
	s_add_i32 s0, s33, s39
	v_lshl_add_u64 v[148:149], v[148:149], 0, s[22:23]
	s_mov_b32 m0, s0
	s_nop 0
	global_load_lds_dwordx4 v[148:149], off
	v_lshl_add_u64 v[148:149], v[208:209], 0, s[22:23]
	s_add_i32 m0, s0, 0x2000
	s_add_i32 s0, s63, s39
	global_load_lds_dwordx4 v[148:149], off
	v_lshl_add_u64 v[148:149], v[224:225], 0, s[22:23]
	s_mov_b32 m0, s0
	s_nop 0
	global_load_lds_dwordx4 v[148:149], off
	v_lshl_add_u64 v[148:149], v[226:227], 0, s[22:23]
	s_add_i32 m0, s0, 0x2000
	s_nop 0
	global_load_lds_dwordx4 v[148:149], off
	s_cmp_ge_i32 s61, s48
	s_cbranch_scc0 .Lkr4_b
	v_lshl_add_u64 v[148:149], v[228:229], 0, s[22:23]
	s_mov_b32 m0, s46
	s_nop 0
	global_load_lds_dwordx4 v[148:149], off
	v_lshl_add_u64 v[148:149], v[230:231], 0, s[22:23]
	s_mov_b32 m0, s47
	s_nop 0
	global_load_lds_dwordx4 v[148:149], off

; #define PG8_STAGE(bufoff, gbase, voff) do { _Pragma("unroll") for (int _i = 0; _i < 2; ++_i) \
;         __builtin_amdgcn_global_load_lds((const unsigned*)((const char*)(gbase) + (voff)[_i]), (PG8_LAS unsigned*)(lds + (bufoff) + ldsw + _i * 8192), 16, 0, 0); } while (0)
; #define PG8_LDA(dst, b, h) do { _Pragma("unroll") for (int m = 0; m < 4; ++m) { const bf16x8 f0_ = *(const PG8_LAS bf16x8*)(lds + PG8_SA(b, h) + aoff + m * 2048), f1_ = *(const PG8_LAS bf16x8*)(lds + PG8_SA(b, h) + aoff + m * 2048 + 1024); dst[m].set(f0_, f1_); } } while (0)
; #define PG8_LDB(dst, b, h) do { _Pragma("unroll") for (int n = 0; n < 2; ++n) { const bf16x8 f0_ = *(const PG8_LAS bf16x8*)(lds + PG8_SB(b, h) + boff + n * 2048), f1_ = *(const PG8_LAS bf16x8*)(lds + PG8_SB(b, h) + boff + n * 2048 + 1024); dst[n].set(f0_, f1_); } } while (0)
; #define PG8_WAIT_V(n) asm volatile("s_waitcnt vmcnt(" #n ")" ::: "memory")
; #define PG8_WAIT_L(n) asm volatile("s_waitcnt lgkmcnt(" #n ")" ::: "memory")
; #define PG8_BAR __builtin_amdgcn_s_barrier()
; #define PG8_SCHED __builtin_amdgcn_sched_barrier(0)
; template <class Epi, class Sched, bool ALIGN_EPI = false, bool SP2 = false>
; __device__ __forceinline__ void gemm_phase(PG8_LAS unsigned char* lds, const Gemm g, const Sched& S, const Epi& E) {
;     ...
;             const bool last = (t == nt - 2);
;             const char* a1 = cA + (size_t)(t + 1) * kstep;
;             const char* a2 = last ? nA : cA + (size_t)(t + 2) * kstep; const char* b2 = last ? nB : cB + (size_t)(t + 2) * kstep;
;             const char* a3 = a2 + kstep; const char* b3 = b2 + kstep;
;             if (last && has_next) S.a_ready(nxt);
;             if constexpr (SP2) {
;             PG8_LDB(B0, 0, 0); PG8_LDB(B1, 0, 1); PG8_SCHED; PG8_LDA(At, 0, 0); PG8_STAGE(PG8_SA(1, 1), a1 + hstep, voffA);
;             PG8_WAIT_V(8); PG8_WAIT_L(0); PG8_BAR; PG8_MMA(0, 0, At, B0); PG8_MMA(0, 1, At, B1); PG8_BAR; PG8_SCHED;
;             PG8_LDA(At, 0, 1); PG8_STAGE(PG8_SB(0, 0), b2, voffB); PG8_STAGE(PG8_SB(0, 1), b2 + hstepB, voffB); PG8_STAGE(PG8_SA(0, 0), a2, voffA);
;             PG8_WAIT_V(8); PG8_WAIT_L(0); PG8_BAR; PG8_MMA(1, 0, At, B0); PG8_MMA(1, 1, At, B1); PG8_BAR; PG8_SCHED;
.LBB0_1625:
	ds_read_b128 v[18:21], v197
	ds_read_b128 v[22:25], v197 offset:1024
	ds_read_b128 v[26:29], v197 offset:2048
	ds_read_b128 v[30:33], v197 offset:3072
	ds_read_b128 v[2:5], v198
	ds_read_b128 v[6:9], v198 offset:1024
	ds_read_b128 v[10:13], v198 offset:2048
	ds_read_b128 v[14:17], v198 offset:3072
	ds_read_b128 v[184:187], v199
	ds_read_b128 v[188:191], v199 offset:1024
	ds_read_b128 v[212:215], v199 offset:2048
	ds_read_b128 v[216:219], v199 offset:3072
	ds_read_b128 v[220:223], v199 offset:4096
	ds_read_b128 v[224:227], v199 offset:5120
	ds_read_b128 v[228:231], v199 offset:6144
	ds_read_b128 v[232:235], v199 offset:7168
	s_add_i32 s82, s48, 2
	s_add_u32 s0, s46, 0x80
	s_addc_u32 s1, s47, 0
	s_cmp_eq_u32 s66, s48
	s_cselect_b32 s48, s2, s0
	s_cselect_b32 s49, s3, s1
	s_cselect_b32 s51, s45, s81
	s_cselect_b32 s50, s44, s80
	s_cmp_eq_u32 s99, 0
	s_cbranch_scc1 .Lkr5_a
	v_lshl_add_u64 v[192:193], v[192:193], 0, s[28:29]
	s_mov_b32 m0, s56
	v_lshl_add_u64 v[194:195], v[194:195], 0, s[28:29]
	global_load_lds_dwordx4 v[192:193], off
	s_mov_b32 m0, s57
	s_nop 0
	global_load_lds_dwordx4 v[194:195], off
.Lkr5_a:
	v_lshl_add_u64 v[192:193], s[46:47], 0, v[176:177]
	s_add_i32 m0, s10, 0xc000
	s_nop 0
	global_load_lds_dwordx4 v[192:193], off
	v_lshl_add_u64 v[192:193], s[46:47], 0, v[178:179]
	s_add_i32 m0, s10, 0xe000
	s_nop 0
	global_load_lds_dwordx4 v[192:193], off
	s_waitcnt vmcnt(8)
	s_waitcnt lgkmcnt(0)
	s_barrier
	s_setprio 1
	s_waitcnt lgkmcnt(0)
	v_mfma_scale_f32_16x16x128_f8f6f4 v[158:161], v[18:25], v[184:191], v[158:161], v200, v201 op_sel_hi:[0,0,0]
	v_mfma_scale_f32_16x16x128_f8f6f4 v[154:157], v[26:33], v[184:191], v[154:157], v200, v201 op_sel_hi:[0,0,0]
	v_mfma_scale_f32_16x16x128_f8f6f4 v[142:145], v[18:25], v[212:219], v[142:145], v200, v201 op_sel_hi:[0,0,0]
	v_mfma_scale_f32_16x16x128_f8f6f4 v[138:141], v[26:33], v[212:219], v[138:141], v200, v201 op_sel_hi:[0,0,0]
	v_mfma_scale_f32_16x16x128_f8f6f4 v[126:129], v[18:25], v[220:227], v[126:129], v200, v201 op_sel_hi:[0,0,0]
	v_mfma_scale_f32_16x16x128_f8f6f4 v[122:125], v[26:33], v[220:227], v[122:125], v200, v201 op_sel_hi:[0,0,0]
	v_mfma_scale_f32_16x16x128_f8f6f4 v[110:113], v[18:25], v[228:235], v[110:113], v200, v201 op_sel_hi:[0,0,0]
	v_mfma_scale_f32_16x16x128_f8f6f4 v[106:109], v[26:33], v[228:235], v[106:109], v200, v201 op_sel_hi:[0,0,0]
	s_setprio 0
	s_setprio 1
	v_mfma_scale_f32_16x16x128_f8f6f4 v[150:153], v[2:9], v[184:191], v[150:153], v200, v201 op_sel_hi:[0,0,0]
	v_mfma_scale_f32_16x16x128_f8f6f4 v[146:149], v[10:17], v[184:191], v[146:149], v200, v201 op_sel_hi:[0,0,0]
	v_mfma_scale_f32_16x16x128_f8f6f4 v[134:137], v[2:9], v[212:219], v[134:137], v200, v201 op_sel_hi:[0,0,0]
	v_mfma_scale_f32_16x16x128_f8f6f4 v[130:133], v[10:17], v[212:219], v[130:133], v200, v201 op_sel_hi:[0,0,0]
	v_mfma_scale_f32_16x16x128_f8f6f4 v[118:121], v[2:9], v[220:227], v[118:121], v200, v201 op_sel_hi:[0,0,0]
	v_mfma_scale_f32_16x16x128_f8f6f4 v[114:117], v[10:17], v[220:227], v[114:117], v200, v201 op_sel_hi:[0,0,0]
	v_mfma_scale_f32_16x16x128_f8f6f4 v[102:105], v[2:9], v[228:235], v[102:105], v200, v201 op_sel_hi:[0,0,0]
	v_mfma_scale_f32_16x16x128_f8f6f4 v[98:101], v[10:17], v[228:235], v[98:101], v200, v201 op_sel_hi:[0,0,0]
	s_setprio 0
	s_barrier
	ds_read_b128 v[212:215], v199 offset:16384
	ds_read_b128 v[216:219], v199 offset:17408
	ds_read_b128 v[220:223], v199 offset:18432
	ds_read_b128 v[224:227], v199 offset:19456
	ds_read_b128 v[228:231], v199 offset:20480
	ds_read_b128 v[232:235], v199 offset:21504
	ds_read_b128 v[236:239], v199 offset:22528
	ds_read_b128 v[240:243], v199 offset:23552
	s_add_i32 s0, s73, s9
	v_lshl_add_u64 v[184:185], s[50:51], 0, v[164:165]
	s_mov_b32 m0, s0
	s_nop 0
	global_load_lds_dwordx4 v[184:185], off
	s_add_i32 m0, s0, 0x2000
	s_add_u32 s0, s50, s14
	v_lshl_add_u64 v[186:187], s[50:51], 0, v[168:169]
	s_addc_u32 s1, s51, s15
	s_add_i32 s33, s74, s9
	global_load_lds_dwordx4 v[186:187], off
	v_lshl_add_u64 v[188:189], s[0:1], 0, v[164:165]
	s_mov_b32 m0, s33
	v_lshl_add_u64 v[190:191], s[0:1], 0, v[168:169]
	global_load_lds_dwordx4 v[188:189], off
	s_add_i32 m0, s33, 0x2000
	v_lshl_add_u64 v[192:193], s[48:49], 0, v[162:163]
	global_load_lds_dwordx4 v[190:191], off
	v_lshl_add_u64 v[194:195], s[48:49], 0, v[166:167]
	s_waitcnt vmcnt(6)
	s_waitcnt lgkmcnt(0)
	s_barrier
; #define PG8_STAGE(bufoff, gbase, voff) do { _Pragma("unroll") for (int _i = 0; _i < 2; ++_i) \
;         __builtin_amdgcn_global_load_lds((const unsigned*)((const char*)(gbase) + (voff)[_i]), (PG8_LAS unsigned*)(lds + (bufoff) + ldsw + _i * 8192), 16, 0, 0); } while (0)
; #define PG8_LDA(dst, b, h) do { _Pragma("unroll") for (int m = 0; m < 4; ++m) { const bf16x8 f0_ = *(const PG8_LAS bf16x8*)(lds + PG8_SA(b, h) + aoff + m * 2048), f1_ = *(const PG8_LAS bf16x8*)(lds + PG8_SA(b, h) + aoff + m * 2048 + 1024); dst[m].set(f0_, f1_); } } while (0)
; #define PG8_LDB(dst, b, h) do { _Pragma("unroll") for (int n = 0; n < 2; ++n) { const bf16x8 f0_ = *(const PG8_LAS bf16x8*)(lds + PG8_SB(b, h) + boff + n * 2048), f1_ = *(const PG8_LAS bf16x8*)(lds + PG8_SB(b, h) + boff + n * 2048 + 1024); dst[n].set(f0_, f1_); } } while (0)
; #define PG8_WAIT_V(n) asm volatile("s_waitcnt vmcnt(" #n ")" ::: "memory")
; #define PG8_WAIT_L(n) asm volatile("s_waitcnt lgkmcnt(" #n ")" ::: "memory")
; #define PG8_BAR __builtin_amdgcn_s_barrier()
; #define PG8_SCHED __builtin_amdgcn_sched_barrier(0)
; template <class Epi, class Sched, bool ALIGN_EPI = false, bool SP2 = false>
; __device__ __forceinline__ void gemm_phase(PG8_LAS unsigned char* lds, const Gemm g, const Sched& S, const Epi& E) {
;     ...
;             PG8_WAIT_V(8); PG8_WAIT_L(0); PG8_BAR; PG8_MMA(1, 0, At, B0); PG8_MMA(1, 1, At, B1); PG8_BAR; PG8_SCHED;
;             PG8_LDB(B0, 1, 0); PG8_LDB(B1, 1, 1); PG8_SCHED; PG8_LDA(At, 1, 0); PG8_STAGE(PG8_SA(0, 1), a2 + hstep, voffA);
;             PG8_WAIT_V(8); PG8_WAIT_L(0); PG8_BAR; PG8_MMA(0, 0, At, B0); PG8_MMA(0, 1, At, B1); PG8_BAR; PG8_SCHED;
;             PG8_LDA(At, 1, 1); PG8_STAGE(PG8_SB(1, 0), b3, voffB); PG8_STAGE(PG8_SB(1, 1), b3 + hstepB, voffB); PG8_STAGE(PG8_SA(1, 0), a3, voffA);
	s_setprio 1
	s_waitcnt lgkmcnt(0)
	v_mfma_scale_f32_16x16x128_f8f6f4 v[94:97], v[18:25], v[212:219], v[94:97], v200, v201 op_sel_hi:[0,0,0]
	v_mfma_scale_f32_16x16x128_f8f6f4 v[90:93], v[26:33], v[212:219], v[90:93], v200, v201 op_sel_hi:[0,0,0]
	v_mfma_scale_f32_16x16x128_f8f6f4 v[78:81], v[18:25], v[220:227], v[78:81], v200, v201 op_sel_hi:[0,0,0]
	v_mfma_scale_f32_16x16x128_f8f6f4 v[74:77], v[26:33], v[220:227], v[74:77], v200, v201 op_sel_hi:[0,0,0]
	v_mfma_scale_f32_16x16x128_f8f6f4 v[62:65], v[18:25], v[228:235], v[62:65], v200, v201 op_sel_hi:[0,0,0]
	v_mfma_scale_f32_16x16x128_f8f6f4 v[58:61], v[26:33], v[228:235], v[58:61], v200, v201 op_sel_hi:[0,0,0]
	v_mfma_scale_f32_16x16x128_f8f6f4 v[46:49], v[18:25], v[236:243], v[46:49], v200, v201 op_sel_hi:[0,0,0]
	v_mfma_scale_f32_16x16x128_f8f6f4 v[42:45], v[26:33], v[236:243], v[42:45], v200, v201 op_sel_hi:[0,0,0]
	s_setprio 0
	s_setprio 1
	v_mfma_scale_f32_16x16x128_f8f6f4 v[86:89], v[2:9], v[212:219], v[86:89], v200, v201 op_sel_hi:[0,0,0]
	v_mfma_scale_f32_16x16x128_f8f6f4 v[82:85], v[10:17], v[212:219], v[82:85], v200, v201 op_sel_hi:[0,0,0]
	v_mfma_scale_f32_16x16x128_f8f6f4 v[70:73], v[2:9], v[220:227], v[70:73], v200, v201 op_sel_hi:[0,0,0]
	v_mfma_scale_f32_16x16x128_f8f6f4 v[66:69], v[10:17], v[220:227], v[66:69], v200, v201 op_sel_hi:[0,0,0]
	v_mfma_scale_f32_16x16x128_f8f6f4 v[54:57], v[2:9], v[228:235], v[54:57], v200, v201 op_sel_hi:[0,0,0]
	v_mfma_scale_f32_16x16x128_f8f6f4 v[50:53], v[10:17], v[228:235], v[50:53], v200, v201 op_sel_hi:[0,0,0]
	v_mfma_scale_f32_16x16x128_f8f6f4 v[38:41], v[2:9], v[236:243], v[38:41], v200, v201 op_sel_hi:[0,0,0]
	v_mfma_scale_f32_16x16x128_f8f6f4 v[34:37], v[10:17], v[236:243], v[34:37], v200, v201 op_sel_hi:[0,0,0]
	s_setprio 0
	s_barrier
	ds_read_b128 v[212:215], v199 offset:32768
	ds_read_b128 v[216:219], v199 offset:33792
	ds_read_b128 v[220:223], v199 offset:34816
	ds_read_b128 v[224:227], v199 offset:35840
	ds_read_b128 v[228:231], v199 offset:36864
	ds_read_b128 v[232:235], v199 offset:37888
	ds_read_b128 v[236:239], v199 offset:38912
	ds_read_b128 v[240:243], v199 offset:39936
	s_add_i32 s33, 0, 0x18000
	s_add_i32 s50, 0, 0x1c000
	v_add_u32_e32 v14, s33, v173
	v_add_u32_e32 v30, s50, v173
	ds_read_b128 v[2:5], v14
	ds_read_b128 v[6:9], v14 offset:1024
	ds_read_b128 v[10:13], v14 offset:2048
	ds_read_b128 v[14:17], v14 offset:3072
	ds_read_b128 v[18:21], v30
	ds_read_b128 v[22:25], v30 offset:1024
	ds_read_b128 v[26:29], v30 offset:2048
	ds_read_b128 v[30:33], v30 offset:3072
	s_add_u32 s0, s48, s12
	s_addc_u32 s1, s49, s13
	s_mov_b32 m0, s52
	v_lshl_add_u64 v[204:205], s[0:1], 0, v[162:163]
	s_mov_b32 m0, s10
	s_nop 0
	global_load_lds_dwordx4 v[192:193], off
	s_mov_b32 m0, s11
	s_nop 0
	global_load_lds_dwordx4 v[194:195], off
	s_mov_b32 m0, s52
	s_nop 0
	global_load_lds_dwordx4 v[204:205], off
	v_lshl_add_u64 v[204:205], s[0:1], 0, v[166:167]
	s_mov_b32 m0, s53
	s_nop 0
	global_load_lds_dwordx4 v[204:205], off
	s_waitcnt vmcnt(8)
	s_waitcnt lgkmcnt(0)
	s_barrier
	s_setprio 1
	s_waitcnt lgkmcnt(0)
	v_mfma_scale_f32_16x16x128_f8f6f4 v[158:161], v[2:9], v[212:219], v[158:161], v200, v201 op_sel_hi:[0,0,0]
	v_mfma_scale_f32_16x16x128_f8f6f4 v[154:157], v[10:17], v[212:219], v[154:157], v200, v201 op_sel_hi:[0,0,0]
	v_mfma_scale_f32_16x16x128_f8f6f4 v[142:145], v[2:9], v[220:227], v[142:145], v200, v201 op_sel_hi:[0,0,0]
	v_mfma_scale_f32_16x16x128_f8f6f4 v[138:141], v[10:17], v[220:227], v[138:141], v200, v201 op_sel_hi:[0,0,0]
	v_mfma_scale_f32_16x16x128_f8f6f4 v[126:129], v[2:9], v[228:235], v[126:129], v200, v201 op_sel_hi:[0,0,0]
	v_mfma_scale_f32_16x16x128_f8f6f4 v[122:125], v[10:17], v[228:235], v[122:125], v200, v201 op_sel_hi:[0,0,0]
	v_mfma_scale_f32_16x16x128_f8f6f4 v[110:113], v[2:9], v[236:243], v[110:113], v200, v201 op_sel_hi:[0,0,0]
	v_mfma_scale_f32_16x16x128_f8f6f4 v[106:109], v[10:17], v[236:243], v[106:109], v200, v201 op_sel_hi:[0,0,0]
	s_setprio 0
	s_setprio 1
	v_mfma_scale_f32_16x16x128_f8f6f4 v[150:153], v[18:25], v[212:219], v[150:153], v200, v201 op_sel_hi:[0,0,0]
	v_mfma_scale_f32_16x16x128_f8f6f4 v[146:149], v[26:33], v[212:219], v[146:149], v200, v201 op_sel_hi:[0,0,0]
	v_mfma_scale_f32_16x16x128_f8f6f4 v[134:137], v[18:25], v[220:227], v[134:137], v200, v201 op_sel_hi:[0,0,0]
	v_mfma_scale_f32_16x16x128_f8f6f4 v[130:133], v[26:33], v[220:227], v[130:133], v200, v201 op_sel_hi:[0,0,0]
	v_mfma_scale_f32_16x16x128_f8f6f4 v[118:121], v[18:25], v[228:235], v[118:121], v200, v201 op_sel_hi:[0,0,0]
	v_mfma_scale_f32_16x16x128_f8f6f4 v[114:117], v[26:33], v[228:235], v[114:117], v200, v201 op_sel_hi:[0,0,0]
	v_mfma_scale_f32_16x16x128_f8f6f4 v[102:105], v[18:25], v[236:243], v[102:105], v200, v201 op_sel_hi:[0,0,0]
	v_mfma_scale_f32_16x16x128_f8f6f4 v[98:101], v[26:33], v[236:243], v[98:101], v200, v201 op_sel_hi:[0,0,0]
	s_setprio 0
	s_barrier
	ds_read_b128 v[212:215], v199 offset:49152
	ds_read_b128 v[216:219], v199 offset:50176
	ds_read_b128 v[220:223], v199 offset:51200
	ds_read_b128 v[224:227], v199 offset:52224
	ds_read_b128 v[228:231], v199 offset:53248
	ds_read_b128 v[232:235], v199 offset:54272
	ds_read_b128 v[236:239], v199 offset:55296
	ds_read_b128 v[240:243], v199 offset:56320
	s_add_i32 s0, s33, s9
	v_lshl_add_u64 v[184:185], v[184:185], 0, s[28:29]
	s_mov_b32 m0, s0
	s_nop 0
	global_load_lds_dwordx4 v[184:185], off
	v_lshl_add_u64 v[184:185], v[186:187], 0, s[28:29]
	s_add_i32 m0, s0, 0x2000
	s_add_i32 s0, s50, s9
	global_load_lds_dwordx4 v[184:185], off
	v_lshl_add_u64 v[184:185], v[188:189], 0, s[28:29]
	s_mov_b32 m0, s0
	s_nop 0
	global_load_lds_dwordx4 v[184:185], off
	v_lshl_add_u64 v[184:185], v[190:191], 0, s[28:29]
	s_add_i32 m0, s0, 0x2000
	s_nop 0
	global_load_lds_dwordx4 v[184:185], off
	s_cmp_ge_i32 s82, s58
	s_cbranch_scc0 .Lkr5_b
	v_lshl_add_u64 v[184:185], v[192:193], 0, s[28:29]
	s_mov_b32 m0, s56
	s_nop 0
	global_load_lds_dwordx4 v[184:185], off
	v_lshl_add_u64 v[184:185], v[194:195], 0, s[28:29]
	s_mov_b32 m0, s57
	s_nop 0
	global_load_lds_dwordx4 v[184:185], off

; #define PG8_STAGE(bufoff, gbase, voff) do { _Pragma("unroll") for (int _i = 0; _i < 2; ++_i) \
;         __builtin_amdgcn_global_load_lds((const unsigned*)((const char*)(gbase) + (voff)[_i]), (PG8_LAS unsigned*)(lds + (bufoff) + ldsw + _i * 8192), 16, 0, 0); } while (0)
; #define PG8_LDA(dst, b, h) do { _Pragma("unroll") for (int m = 0; m < 4; ++m) { const bf16x8 f0_ = *(const PG8_LAS bf16x8*)(lds + PG8_SA(b, h) + aoff + m * 2048), f1_ = *(const PG8_LAS bf16x8*)(lds + PG8_SA(b, h) + aoff + m * 2048 + 1024); dst[m].set(f0_, f1_); } } while (0)
; #define PG8_LDB(dst, b, h) do { _Pragma("unroll") for (int n = 0; n < 2; ++n) { const bf16x8 f0_ = *(const PG8_LAS bf16x8*)(lds + PG8_SB(b, h) + boff + n * 2048), f1_ = *(const PG8_LAS bf16x8*)(lds + PG8_SB(b, h) + boff + n * 2048 + 1024); dst[n].set(f0_, f1_); } } while (0)
; #define PG8_WAIT_V(n) asm volatile("s_waitcnt vmcnt(" #n ")" ::: "memory")
; #define PG8_WAIT_L(n) asm volatile("s_waitcnt lgkmcnt(" #n ")" ::: "memory")
; #define PG8_BAR __builtin_amdgcn_s_barrier()
; #define PG8_SCHED __builtin_amdgcn_sched_barrier(0)
; template <class Epi, class Sched, bool ALIGN_EPI = false, bool SP2 = false>
; __device__ __forceinline__ void gemm_phase(PG8_LAS unsigned char* lds, const Gemm g, const Sched& S, const Epi& E) {
;     ...
;             const bool last = (t == nt - 2);
;             const char* a1 = cA + (size_t)(t + 1) * kstep;
;             const char* a2 = last ? nA : cA + (size_t)(t + 2) * kstep; const char* b2 = last ? nB : cB + (size_t)(t + 2) * kstep;
;             const char* a3 = a2 + kstep; const char* b3 = b2 + kstep;
;             if (last && has_next) S.a_ready(nxt);
;             if constexpr (SP2) {
;             PG8_LDB(B0, 0, 0); PG8_LDB(B1, 0, 1); PG8_SCHED; PG8_LDA(At, 0, 0); PG8_STAGE(PG8_SA(1, 1), a1 + hstep, voffA);
;             PG8_WAIT_V(8); PG8_WAIT_L(0); PG8_BAR; PG8_MMA(0, 0, At, B0); PG8_MMA(0, 1, At, B1); PG8_BAR; PG8_SCHED;
;             PG8_LDA(At, 0, 1); PG8_STAGE(PG8_SB(0, 0), b2, voffB); PG8_STAGE(PG8_SB(0, 1), b2 + hstepB, voffB); PG8_STAGE(PG8_SA(0, 0), a2, voffA);
;             PG8_WAIT_V(8); PG8_WAIT_L(0); PG8_BAR; PG8_MMA(1, 0, At, B0); PG8_MMA(1, 1, At, B1); PG8_BAR; PG8_SCHED;
.LBB0_1658:
	ds_read_b128 v[16:19], v215
	ds_read_b128 v[20:23], v215 offset:1024
	ds_read_b128 v[24:27], v215 offset:2048
	ds_read_b128 v[28:31], v215 offset:3072
	ds_read_b128 v[0:3], v216
	ds_read_b128 v[4:7], v216 offset:1024
	ds_read_b128 v[8:11], v216 offset:2048
	ds_read_b128 v[12:15], v216 offset:3072
	ds_read_b128 v[152:155], v217
	ds_read_b128 v[156:159], v217 offset:1024
	ds_read_b128 v[172:175], v217 offset:3072
	ds_read_b128 v[176:179], v217 offset:4096
	ds_read_b128 v[180:183], v217 offset:5120
	ds_read_b128 v[226:229], v217 offset:6144
	ds_read_b128 v[230:233], v217 offset:7168
	s_add_i32 s83, s78, 2
	s_add_u32 s0, s2, 0x80
	s_addc_u32 s1, s3, 0
	s_cmp_eq_u32 s97, s78
	s_cselect_b32 s78, s58, s0
	s_cselect_b32 s79, s59, s1
	s_cselect_b32 s81, s75, s82
	s_cselect_b32 s80, s74, s57
	s_cmp_eq_u32 s99, 0
	s_cbranch_scc1 .Lkr6_a
	v_lshl_add_u64 v[168:169], v[168:169], 0, s[36:37]
	s_mov_b32 m0, s93
	v_lshl_add_u64 v[170:171], v[170:171], 0, s[36:37]
	global_load_lds_dwordx4 v[168:169], off
	s_mov_b32 m0, s94
	s_nop 0
	global_load_lds_dwordx4 v[170:171], off
.Lkr6_a:
	v_lshl_add_u64 v[206:207], s[2:3], 0, v[198:199]
	s_add_i32 m0, s71, 0xc000
	ds_read_b128 v[168:171], v217 offset:2048
	global_load_lds_dwordx4 v[206:207], off
	v_lshl_add_u64 v[206:207], s[2:3], 0, v[200:201]
	s_add_i32 m0, s71, 0xe000
	s_nop 0
	global_load_lds_dwordx4 v[206:207], off
	s_waitcnt vmcnt(8)
	s_waitcnt lgkmcnt(0)
	s_barrier
	s_setprio 1
	s_waitcnt lgkmcnt(0)
	v_mfma_scale_f32_16x16x128_f8f6f4 v[164:167], v[16:23], v[152:159], v[164:167], v218, v219 op_sel_hi:[0,0,0]
	v_mfma_scale_f32_16x16x128_f8f6f4 v[160:163], v[24:31], v[152:159], v[160:163], v218, v219 op_sel_hi:[0,0,0]
	v_mfma_scale_f32_16x16x128_f8f6f4 v[140:143], v[16:23], v[168:175], v[140:143], v218, v219 op_sel_hi:[0,0,0]
	v_mfma_scale_f32_16x16x128_f8f6f4 v[136:139], v[24:31], v[168:175], v[136:139], v218, v219 op_sel_hi:[0,0,0]
	v_mfma_scale_f32_16x16x128_f8f6f4 v[108:111], v[16:23], v[176:183], v[108:111], v218, v219 op_sel_hi:[0,0,0]
	v_mfma_scale_f32_16x16x128_f8f6f4 v[104:107], v[24:31], v[176:183], v[104:107], v218, v219 op_sel_hi:[0,0,0]
	v_mfma_scale_f32_16x16x128_f8f6f4 v[116:119], v[16:23], v[226:233], v[116:119], v218, v219 op_sel_hi:[0,0,0]
	v_mfma_scale_f32_16x16x128_f8f6f4 v[112:115], v[24:31], v[226:233], v[112:115], v218, v219 op_sel_hi:[0,0,0]
	s_setprio 0
	s_setprio 1
	v_mfma_scale_f32_16x16x128_f8f6f4 v[148:151], v[0:7], v[152:159], v[148:151], v218, v219 op_sel_hi:[0,0,0]
	v_mfma_scale_f32_16x16x128_f8f6f4 v[144:147], v[8:15], v[152:159], v[144:147], v218, v219 op_sel_hi:[0,0,0]
	v_mfma_scale_f32_16x16x128_f8f6f4 v[132:135], v[0:7], v[168:175], v[132:135], v218, v219 op_sel_hi:[0,0,0]
	v_mfma_scale_f32_16x16x128_f8f6f4 v[128:131], v[8:15], v[168:175], v[128:131], v218, v219 op_sel_hi:[0,0,0]
	v_mfma_scale_f32_16x16x128_f8f6f4 v[124:127], v[0:7], v[176:183], v[124:127], v218, v219 op_sel_hi:[0,0,0]
	v_mfma_scale_f32_16x16x128_f8f6f4 v[120:123], v[8:15], v[176:183], v[120:123], v218, v219 op_sel_hi:[0,0,0]
	v_mfma_scale_f32_16x16x128_f8f6f4 v[100:103], v[0:7], v[226:233], v[100:103], v218, v219 op_sel_hi:[0,0,0]
	v_mfma_scale_f32_16x16x128_f8f6f4 v[96:99], v[8:15], v[226:233], v[96:99], v218, v219 op_sel_hi:[0,0,0]
	s_setprio 0
	s_barrier
	ds_read_b128 v[172:175], v217 offset:16384
	ds_read_b128 v[176:179], v217 offset:17408
	ds_read_b128 v[226:229], v217 offset:18432
	ds_read_b128 v[230:233], v217 offset:19456
	ds_read_b128 v[234:237], v217 offset:20480
	ds_read_b128 v[238:241], v217 offset:21504
	ds_read_b128 v[242:245], v217 offset:22528
	ds_read_b128 v[246:249], v217 offset:23552
	s_add_i32 s0, s67, s45
	v_lshl_add_u64 v[152:153], s[80:81], 0, v[186:187]
	s_mov_b32 m0, s0
	s_nop 0
	global_load_lds_dwordx4 v[152:153], off
	s_add_i32 m0, s0, 0x2000
	s_add_u32 s0, s80, s20
	v_lshl_add_u64 v[154:155], s[80:81], 0, v[190:191]
	s_addc_u32 s1, s81, s21
	s_add_i32 s33, s10, s45
	global_load_lds_dwordx4 v[154:155], off
	v_lshl_add_u64 v[156:157], s[0:1], 0, v[186:187]
	s_mov_b32 m0, s33
	v_lshl_add_u64 v[158:159], s[0:1], 0, v[190:191]
	global_load_lds_dwordx4 v[156:157], off
	s_add_i32 m0, s33, 0x2000
	v_lshl_add_u64 v[168:169], s[78:79], 0, v[184:185]
	global_load_lds_dwordx4 v[158:159], off
	v_lshl_add_u64 v[170:171], s[78:79], 0, v[188:189]
	s_waitcnt vmcnt(6)
	s_waitcnt lgkmcnt(0)
	s_barrier
; #define PG8_STAGE(bufoff, gbase, voff) do { _Pragma("unroll") for (int _i = 0; _i < 2; ++_i) \
;         __builtin_amdgcn_global_load_lds((const unsigned*)((const char*)(gbase) + (voff)[_i]), (PG8_LAS unsigned*)(lds + (bufoff) + ldsw + _i * 8192), 16, 0, 0); } while (0)
; #define PG8_LDA(dst, b, h) do { _Pragma("unroll") for (int m = 0; m < 4; ++m) { const bf16x8 f0_ = *(const PG8_LAS bf16x8*)(lds + PG8_SA(b, h) + aoff + m * 2048), f1_ = *(const PG8_LAS bf16x8*)(lds + PG8_SA(b, h) + aoff + m * 2048 + 1024); dst[m].set(f0_, f1_); } } while (0)
; #define PG8_LDB(dst, b, h) do { _Pragma("unroll") for (int n = 0; n < 2; ++n) { const bf16x8 f0_ = *(const PG8_LAS bf16x8*)(lds + PG8_SB(b, h) + boff + n * 2048), f1_ = *(const PG8_LAS bf16x8*)(lds + PG8_SB(b, h) + boff + n * 2048 + 1024); dst[n].set(f0_, f1_); } } while (0)
; #define PG8_WAIT_V(n) asm volatile("s_waitcnt vmcnt(" #n ")" ::: "memory")
; #define PG8_WAIT_L(n) asm volatile("s_waitcnt lgkmcnt(" #n ")" ::: "memory")
; #define PG8_BAR __builtin_amdgcn_s_barrier()
; #define PG8_SCHED __builtin_amdgcn_sched_barrier(0)
; template <class Epi, class Sched, bool ALIGN_EPI = false, bool SP2 = false>
; __device__ __forceinline__ void gemm_phase(PG8_LAS unsigned char* lds, const Gemm g, const Sched& S, const Epi& E) {
;     ...
;             PG8_WAIT_V(8); PG8_WAIT_L(0); PG8_BAR; PG8_MMA(1, 0, At, B0); PG8_MMA(1, 1, At, B1); PG8_BAR; PG8_SCHED;
;             PG8_LDB(B0, 1, 0); PG8_LDB(B1, 1, 1); PG8_SCHED; PG8_LDA(At, 1, 0); PG8_STAGE(PG8_SA(0, 1), a2 + hstep, voffA);
;             PG8_WAIT_V(8); PG8_WAIT_L(0); PG8_BAR; PG8_MMA(0, 0, At, B0); PG8_MMA(0, 1, At, B1); PG8_BAR; PG8_SCHED;
;             PG8_LDA(At, 1, 1); PG8_STAGE(PG8_SB(1, 0), b3, voffB); PG8_STAGE(PG8_SB(1, 1), b3 + hstepB, voffB); PG8_STAGE(PG8_SA(1, 0), a3, voffA);
	s_setprio 1
	s_waitcnt lgkmcnt(0)
	v_mfma_scale_f32_16x16x128_f8f6f4 v[92:95], v[16:23], v[172:179], v[92:95], v218, v219 op_sel_hi:[0,0,0]
	v_mfma_scale_f32_16x16x128_f8f6f4 v[88:91], v[24:31], v[172:179], v[88:91], v218, v219 op_sel_hi:[0,0,0]
	v_mfma_scale_f32_16x16x128_f8f6f4 v[76:79], v[16:23], v[226:233], v[76:79], v218, v219 op_sel_hi:[0,0,0]
	v_mfma_scale_f32_16x16x128_f8f6f4 v[72:75], v[24:31], v[226:233], v[72:75], v218, v219 op_sel_hi:[0,0,0]
	v_mfma_scale_f32_16x16x128_f8f6f4 v[60:63], v[16:23], v[234:241], v[60:63], v218, v219 op_sel_hi:[0,0,0]
	v_mfma_scale_f32_16x16x128_f8f6f4 v[56:59], v[24:31], v[234:241], v[56:59], v218, v219 op_sel_hi:[0,0,0]
	v_mfma_scale_f32_16x16x128_f8f6f4 v[44:47], v[16:23], v[242:249], v[44:47], v218, v219 op_sel_hi:[0,0,0]
	v_mfma_scale_f32_16x16x128_f8f6f4 v[40:43], v[24:31], v[242:249], v[40:43], v218, v219 op_sel_hi:[0,0,0]
	s_setprio 0
	s_setprio 1
	v_mfma_scale_f32_16x16x128_f8f6f4 v[84:87], v[0:7], v[172:179], v[84:87], v218, v219 op_sel_hi:[0,0,0]
	v_mfma_scale_f32_16x16x128_f8f6f4 v[80:83], v[8:15], v[172:179], v[80:83], v218, v219 op_sel_hi:[0,0,0]
	v_mfma_scale_f32_16x16x128_f8f6f4 v[68:71], v[0:7], v[226:233], v[68:71], v218, v219 op_sel_hi:[0,0,0]
	v_mfma_scale_f32_16x16x128_f8f6f4 v[64:67], v[8:15], v[226:233], v[64:67], v218, v219 op_sel_hi:[0,0,0]
	v_mfma_scale_f32_16x16x128_f8f6f4 v[52:55], v[0:7], v[234:241], v[52:55], v218, v219 op_sel_hi:[0,0,0]
	v_mfma_scale_f32_16x16x128_f8f6f4 v[48:51], v[8:15], v[234:241], v[48:51], v218, v219 op_sel_hi:[0,0,0]
	v_mfma_scale_f32_16x16x128_f8f6f4 v[36:39], v[0:7], v[242:249], v[36:39], v218, v219 op_sel_hi:[0,0,0]
	v_mfma_scale_f32_16x16x128_f8f6f4 v[32:35], v[8:15], v[242:249], v[32:35], v218, v219 op_sel_hi:[0,0,0]
	s_setprio 0
	s_barrier
	ds_read_b128 v[172:175], v217 offset:32768
	ds_read_b128 v[176:179], v217 offset:33792
	ds_read_b128 v[226:229], v217 offset:34816
	ds_read_b128 v[230:233], v217 offset:35840
	ds_read_b128 v[234:237], v217 offset:36864
	ds_read_b128 v[238:241], v217 offset:37888
	ds_read_b128 v[242:245], v217 offset:38912
	ds_read_b128 v[246:249], v217 offset:39936
	s_add_i32 s33, 0, 0x18000
	s_add_i32 s80, 0, 0x1c000
	v_add_u32_e32 v12, s33, v211
	v_add_u32_e32 v28, s80, v211
	ds_read_b128 v[0:3], v12
	ds_read_b128 v[4:7], v12 offset:1024
	ds_read_b128 v[8:11], v12 offset:2048
	ds_read_b128 v[12:15], v12 offset:3072
	ds_read_b128 v[16:19], v28
	ds_read_b128 v[20:23], v28 offset:1024
	ds_read_b128 v[24:27], v28 offset:2048
	ds_read_b128 v[28:31], v28 offset:3072
	s_add_u32 s0, s78, s18
	s_addc_u32 s1, s79, s19
	s_mov_b32 m0, s86
	v_lshl_add_u64 v[180:181], s[0:1], 0, v[184:185]
	s_mov_b32 m0, s71
	s_nop 0
	global_load_lds_dwordx4 v[168:169], off
	s_mov_b32 m0, s73
	s_nop 0
	global_load_lds_dwordx4 v[170:171], off
	s_mov_b32 m0, s86
	s_nop 0
	global_load_lds_dwordx4 v[180:181], off
	v_lshl_add_u64 v[180:181], s[0:1], 0, v[188:189]
	s_mov_b32 m0, s87
	s_nop 0
	global_load_lds_dwordx4 v[180:181], off
	s_waitcnt vmcnt(8)
	s_waitcnt lgkmcnt(0)
	s_barrier
	s_setprio 1
	s_waitcnt lgkmcnt(0)
	v_mfma_scale_f32_16x16x128_f8f6f4 v[164:167], v[0:7], v[172:179], v[164:167], v218, v219 op_sel_hi:[0,0,0]
	v_mfma_scale_f32_16x16x128_f8f6f4 v[160:163], v[8:15], v[172:179], v[160:163], v218, v219 op_sel_hi:[0,0,0]
	v_mfma_scale_f32_16x16x128_f8f6f4 v[140:143], v[0:7], v[226:233], v[140:143], v218, v219 op_sel_hi:[0,0,0]
	v_mfma_scale_f32_16x16x128_f8f6f4 v[136:139], v[8:15], v[226:233], v[136:139], v218, v219 op_sel_hi:[0,0,0]
	v_mfma_scale_f32_16x16x128_f8f6f4 v[108:111], v[0:7], v[234:241], v[108:111], v218, v219 op_sel_hi:[0,0,0]
	v_mfma_scale_f32_16x16x128_f8f6f4 v[104:107], v[8:15], v[234:241], v[104:107], v218, v219 op_sel_hi:[0,0,0]
	v_mfma_scale_f32_16x16x128_f8f6f4 v[116:119], v[0:7], v[242:249], v[116:119], v218, v219 op_sel_hi:[0,0,0]
	v_mfma_scale_f32_16x16x128_f8f6f4 v[112:115], v[8:15], v[242:249], v[112:115], v218, v219 op_sel_hi:[0,0,0]
	s_setprio 0
	s_setprio 1
	v_mfma_scale_f32_16x16x128_f8f6f4 v[148:151], v[16:23], v[172:179], v[148:151], v218, v219 op_sel_hi:[0,0,0]
	v_mfma_scale_f32_16x16x128_f8f6f4 v[144:147], v[24:31], v[172:179], v[144:147], v218, v219 op_sel_hi:[0,0,0]
	v_mfma_scale_f32_16x16x128_f8f6f4 v[132:135], v[16:23], v[226:233], v[132:135], v218, v219 op_sel_hi:[0,0,0]
	v_mfma_scale_f32_16x16x128_f8f6f4 v[128:131], v[24:31], v[226:233], v[128:131], v218, v219 op_sel_hi:[0,0,0]
	v_mfma_scale_f32_16x16x128_f8f6f4 v[124:127], v[16:23], v[234:241], v[124:127], v218, v219 op_sel_hi:[0,0,0]
	v_mfma_scale_f32_16x16x128_f8f6f4 v[120:123], v[24:31], v[234:241], v[120:123], v218, v219 op_sel_hi:[0,0,0]
	v_mfma_scale_f32_16x16x128_f8f6f4 v[100:103], v[16:23], v[242:249], v[100:103], v218, v219 op_sel_hi:[0,0,0]
	v_mfma_scale_f32_16x16x128_f8f6f4 v[96:99], v[24:31], v[242:249], v[96:99], v218, v219 op_sel_hi:[0,0,0]
	s_setprio 0
	s_barrier
	ds_read_b128 v[172:175], v217 offset:49152
	ds_read_b128 v[176:179], v217 offset:50176
	ds_read_b128 v[226:229], v217 offset:51200
	ds_read_b128 v[230:233], v217 offset:52224
	ds_read_b128 v[234:237], v217 offset:53248
	ds_read_b128 v[238:241], v217 offset:54272
	ds_read_b128 v[242:245], v217 offset:55296
	ds_read_b128 v[246:249], v217 offset:56320
	s_add_i32 s0, s33, s45
	v_lshl_add_u64 v[152:153], v[152:153], 0, s[36:37]
	s_mov_b32 m0, s0
	s_nop 0
	global_load_lds_dwordx4 v[152:153], off
	v_lshl_add_u64 v[152:153], v[154:155], 0, s[36:37]
	s_add_i32 m0, s0, 0x2000
	s_add_i32 s0, s80, s45
	global_load_lds_dwordx4 v[152:153], off
	v_lshl_add_u64 v[152:153], v[156:157], 0, s[36:37]
	s_mov_b32 m0, s0
	s_nop 0
	global_load_lds_dwordx4 v[152:153], off
	v_lshl_add_u64 v[152:153], v[158:159], 0, s[36:37]
	s_add_i32 m0, s0, 0x2000
	s_nop 0
	global_load_lds_dwordx4 v[152:153], off
	s_cmp_ge_i32 s83, s91
	s_cbranch_scc0 .Lkr6_b
	v_lshl_add_u64 v[152:153], v[168:169], 0, s[36:37]
	s_mov_b32 m0, s93
	s_nop 0
	global_load_lds_dwordx4 v[152:153], off
	v_lshl_add_u64 v[152:153], v[170:171], 0, s[36:37]
	s_mov_b32 m0, s94
	s_nop 0
	global_load_lds_dwordx4 v[152:153], off
